# v60 + ds_read issue interleaved with LDS-DMA issue in the 6-DMA load segments of the bf16 GEMM K-loops (P1, P5a, P5r, P6)
# speedup vs baseline: 1.0033x; 1.0033x over previous
; #define LAS __attribute__((address_space(3)))
; #define PG8_STAGEB(bufoff, gbase) PG8_STAGE2(bufoff, gbase, voffB[0], voffB[1])
; #define PG8_STAGEA(bufoff, gbase, h) PG8_STAGE2(bufoff, gbase, voffA[h][0], voffA[h][1])
; #define PG8_STAGEAS(bufoff, gbase, h) PG8_STAGE2(bufoff, gbase, voffA[h][0], voffA[h][1])
; #define PG8_LDA(dst, b, h) do { _Pragma("unroll") for (int m = 0; m < 4; ++m) _Pragma("unroll") for (int k = 0; k < 2; ++k) dst[m][k] = *(const LAS bf16x8*)(lds + PG8_SA(b, h) + aoff + m * 2048 + k * 1024); } while (0)
; #define PG8_LDB(dst, b, h) do { _Pragma("unroll") for (int n = 0; n < 2; ++n) _Pragma("unroll") for (int k = 0; k < 2; ++k) dst[n][k] = *(const LAS bf16x8*)(lds + PG8_SB(b, h) + boff + n * 2048 + k * 1024); } while (0)
; #define PG8_WAIT_K() do { if constexpr (HM) PG8_WAIT_V(6); else PG8_WAIT_V(8); } while (0)
; #define PG8_WAIT_K0() do { if (EST > 0 && t == 0 && ui > 0) asm volatile("s_waitcnt vmcnt(%0)" :: "n"((HM ? 6 : 8) + EST) : "memory"); else PG8_WAIT_K(); } while (0)
; #define PG8_WAIT_L(n) asm volatile("s_waitcnt lgkmcnt(" #n ")" ::: "memory")
; #define PG8_BAR __builtin_amdgcn_s_barrier()
; #define PG8_SCHED __builtin_amdgcn_sched_barrier(0)
;     ...
;             PG8_LDB(B0, 0, 0); PG8_LDB(B1, 0, 1); PG8_SCHED; PG8_LDA(At, 0, 0); if constexpr (!HM) PG8_STAGEA(PG8_SA(1, 1), a1, 1);
;             if constexpr (Sched::kGather) { if (last && has_next) { const u32x4 tn = *(const LAS u32x4*)(S.aux + tid * 16); voffA[0][0] = tn.x; voffA[0][1] = tn.y; voffA[1][0] = tn.z; voffA[1][1] = tn.w; } }
;             PG8_WAIT_K0(); PG8_WAIT_L(0); PG8_BAR; PG8_MMA(0, 0, At, B0); PG8_MMA(0, 1, At, B1); PG8_BAR; PG8_SCHED;
;             if constexpr (!HM) PG8_LDA(At, 0, 1);
;             PG8_STAGEB(PG8_SB(0, 0), b2); PG8_STAGEB(PG8_SB(0, 1), b2 + hstepB); PG8_STAGEAS(PG8_SA(0, 0), a2, 0);
;             PG8_WAIT_K0(); PG8_WAIT_L(0); PG8_BAR; if constexpr (!HM) { PG8_MMA(1, 0, At, B0); PG8_MMA(1, 1, At, B1); } PG8_BAR; PG8_SCHED;
;             PG8_LDB(B0, 1, 0); PG8_LDB(B1, 1, 1); PG8_SCHED; PG8_LDA(At, 1, 0); if constexpr (!HM) PG8_STAGEAS(PG8_SA(0, 1), a2, 1);
;             PG8_WAIT_K(); PG8_WAIT_L(0); PG8_BAR; PG8_MMA(0, 0, At, B0); PG8_MMA(0, 1, At, B1); PG8_BAR; PG8_SCHED;
;             if constexpr (!HM) PG8_LDA(At, 1, 1);
;             PG8_STAGEB(PG8_SB(1, 0), b3); PG8_STAGEB(PG8_SB(1, 1), b3 + hstepB); PG8_STAGEAS(PG8_SA(1, 0), a3, 0);
.LBB0_140:
	ds_read_b128 v[142:145], v163
	ds_read_b128 v[146:149], v163 offset:1024
	ds_read_b128 v[150:153], v163 offset:2048
	ds_read_b128 v[170:173], v163 offset:3072
	ds_read_b128 v[174:177], v164
	ds_read_b128 v[178:181], v164 offset:1024
	ds_read_b128 v[182:185], v164 offset:2048
	ds_read_b128 v[186:189], v164 offset:3072
	s_cmp_eq_u32 s47, 28
	s_cselect_b32 s56, s48, s4
	s_cselect_b32 s57, s49, s11
	s_cselect_b32 s54, s50, s33
	s_cselect_b32 s55, s51, s45
	s_add_u32 s12, s56, 0x80
	s_addc_u32 s13, s57, 0
	ds_read_b128 v[190:193], v165
	ds_read_b128 v[194:197], v165 offset:1024
	ds_read_b128 v[198:201], v165 offset:2048
	ds_read_b128 v[202:205], v165 offset:3072
	ds_read_b128 v[206:209], v165 offset:4096
	ds_read_b128 v[210:213], v165 offset:5120
	ds_read_b128 v[214:217], v165 offset:6144
	ds_read_b128 v[218:221], v165 offset:7168
	s_mov_b32 s80, m0
	s_mov_b32 m0, s72
	s_nop 0
	global_load_lds_dwordx4 v159, s[0:1]
	s_mov_b32 m0, s80
	s_nop 0
	s_mov_b32 s80, m0
	s_mov_b32 m0, s73
	s_nop 0
	global_load_lds_dwordx4 v160, s[0:1]
	s_mov_b32 m0, s80
	s_waitcnt vmcnt(8)
	s_waitcnt lgkmcnt(0)
	s_barrier
	s_setprio 1
	s_waitcnt lgkmcnt(7)
	v_mfma_f32_16x16x32_bf16 v[126:129], v[142:145], v[190:193], v[126:129]
	v_mfma_f32_16x16x32_bf16 v[122:125], v[150:153], v[190:193], v[122:125]
	s_waitcnt lgkmcnt(5)
	v_mfma_f32_16x16x32_bf16 v[110:113], v[142:145], v[198:201], v[110:113]
	v_mfma_f32_16x16x32_bf16 v[106:109], v[150:153], v[198:201], v[106:109]
	s_waitcnt lgkmcnt(3)
	v_mfma_f32_16x16x32_bf16 v[94:97], v[142:145], v[206:209], v[94:97]
	v_mfma_f32_16x16x32_bf16 v[90:93], v[150:153], v[206:209], v[90:93]
	s_waitcnt lgkmcnt(1)
	v_mfma_f32_16x16x32_bf16 v[78:81], v[142:145], v[214:217], v[78:81]
	v_mfma_f32_16x16x32_bf16 v[74:77], v[150:153], v[214:217], v[74:77]
	v_mfma_f32_16x16x32_bf16 v[126:129], v[146:149], v[194:197], v[126:129]
	v_mfma_f32_16x16x32_bf16 v[122:125], v[170:173], v[194:197], v[122:125]
	v_mfma_f32_16x16x32_bf16 v[110:113], v[146:149], v[202:205], v[110:113]
	v_mfma_f32_16x16x32_bf16 v[106:109], v[170:173], v[202:205], v[106:109]
	v_mfma_f32_16x16x32_bf16 v[94:97], v[146:149], v[210:213], v[94:97]
	v_mfma_f32_16x16x32_bf16 v[90:93], v[170:173], v[210:213], v[90:93]
	s_waitcnt lgkmcnt(0)
	v_mfma_f32_16x16x32_bf16 v[78:81], v[146:149], v[218:221], v[78:81]
	v_mfma_f32_16x16x32_bf16 v[74:77], v[170:173], v[218:221], v[74:77]
	s_setprio 0
	s_setprio 1
	v_mfma_f32_16x16x32_bf16 v[118:121], v[174:177], v[190:193], v[118:121]
	v_mfma_f32_16x16x32_bf16 v[114:117], v[182:185], v[190:193], v[114:117]
	v_mfma_f32_16x16x32_bf16 v[102:105], v[174:177], v[198:201], v[102:105]
	v_mfma_f32_16x16x32_bf16 v[98:101], v[182:185], v[198:201], v[98:101]
	v_mfma_f32_16x16x32_bf16 v[86:89], v[174:177], v[206:209], v[86:89]
	v_mfma_f32_16x16x32_bf16 v[82:85], v[182:185], v[206:209], v[82:85]
	v_mfma_f32_16x16x32_bf16 v[70:73], v[174:177], v[214:217], v[70:73]
	v_mfma_f32_16x16x32_bf16 v[66:69], v[182:185], v[214:217], v[66:69]
	v_mfma_f32_16x16x32_bf16 v[118:121], v[178:181], v[194:197], v[118:121]
	v_mfma_f32_16x16x32_bf16 v[114:117], v[186:189], v[194:197], v[114:117]
	v_mfma_f32_16x16x32_bf16 v[102:105], v[178:181], v[202:205], v[102:105]
	v_mfma_f32_16x16x32_bf16 v[98:101], v[186:189], v[202:205], v[98:101]
	v_mfma_f32_16x16x32_bf16 v[86:89], v[178:181], v[210:213], v[86:89]
	v_mfma_f32_16x16x32_bf16 v[82:85], v[186:189], v[210:213], v[82:85]
	v_mfma_f32_16x16x32_bf16 v[70:73], v[178:181], v[218:221], v[70:73]
	v_mfma_f32_16x16x32_bf16 v[66:69], v[186:189], v[218:221], v[66:69]
	s_setprio 0
	s_barrier
	ds_read_b128 v[190:193], v165 offset:16384
	ds_read_b128 v[194:197], v165 offset:17408
	s_mov_b32 s80, m0
	s_mov_b32 m0, s41
	s_nop 0
	global_load_lds_dwordx4 v1, s[54:55]
	s_mov_b32 m0, s80
	ds_read_b128 v[198:201], v165 offset:18432
	ds_read_b128 v[202:205], v165 offset:19456
	s_nop 0
	s_mov_b32 s80, m0
	s_mov_b32 m0, s43
	s_nop 0
	global_load_lds_dwordx4 v156, s[54:55]
	s_mov_b32 m0, s80
	ds_read_b128 v[206:209], v165 offset:20480
	ds_read_b128 v[210:213], v165 offset:21504
	s_add_u32 s80, s54, 0x80000
	s_addc_u32 s81, s55, 0
	s_mov_b32 s82, m0
	s_mov_b32 m0, s53
	s_nop 0
	global_load_lds_dwordx4 v1, s[80:81]
	s_mov_b32 m0, s82
	ds_read_b128 v[214:217], v165 offset:22528
	ds_read_b128 v[218:221], v165 offset:23552
	s_nop 0
	s_mov_b32 s82, m0
	s_mov_b32 m0, s58
	s_nop 0
	global_load_lds_dwordx4 v156, s[80:81]
	s_mov_b32 m0, s82
	s_mov_b32 s80, m0
	s_mov_b32 m0, s29
	s_nop 0
	global_load_lds_dwordx4 v157, s[56:57]
	s_mov_b32 m0, s80
	s_nop 0
	s_mov_b32 s80, m0
	s_mov_b32 m0, s59
	s_nop 0
	global_load_lds_dwordx4 v158, s[56:57]
	s_mov_b32 m0, s80
	s_waitcnt vmcnt(8)
	s_waitcnt lgkmcnt(0)
	s_barrier
; #define PG8_STAGEAS(bufoff, gbase, h) PG8_STAGE2(bufoff, gbase, voffA[h][0], voffA[h][1])
; #define PG8_LDA(dst, b, h) do { _Pragma("unroll") for (int m = 0; m < 4; ++m) _Pragma("unroll") for (int k = 0; k < 2; ++k) dst[m][k] = *(const LAS bf16x8*)(lds + PG8_SA(b, h) + aoff + m * 2048 + k * 1024); } while (0)
; #define PG8_LDB(dst, b, h) do { _Pragma("unroll") for (int n = 0; n < 2; ++n) _Pragma("unroll") for (int k = 0; k < 2; ++k) dst[n][k] = *(const LAS bf16x8*)(lds + PG8_SB(b, h) + boff + n * 2048 + k * 1024); } while (0)
; #define PG8_WAIT_K() do { if constexpr (HM) PG8_WAIT_V(6); else PG8_WAIT_V(8); } while (0)
; #define PG8_WAIT_K0() do { if (EST > 0 && t == 0 && ui > 0) asm volatile("s_waitcnt vmcnt(%0)" :: "n"((HM ? 6 : 8) + EST) : "memory"); else PG8_WAIT_K(); } while (0)
; #define PG8_WAIT_L(n) asm volatile("s_waitcnt lgkmcnt(" #n ")" ::: "memory")
; #define PG8_BAR __builtin_amdgcn_s_barrier()
; #define PG8_SCHED __builtin_amdgcn_sched_barrier(0)
;     ...
;             PG8_WAIT_K0(); PG8_WAIT_L(0); PG8_BAR; if constexpr (!HM) { PG8_MMA(1, 0, At, B0); PG8_MMA(1, 1, At, B1); } PG8_BAR; PG8_SCHED;
;             PG8_LDB(B0, 1, 0); PG8_LDB(B1, 1, 1); PG8_SCHED; PG8_LDA(At, 1, 0); if constexpr (!HM) PG8_STAGEAS(PG8_SA(0, 1), a2, 1);
;             PG8_WAIT_K(); PG8_WAIT_L(0); PG8_BAR; PG8_MMA(0, 0, At, B0); PG8_MMA(0, 1, At, B1); PG8_BAR; PG8_SCHED;
	s_setprio 1
	s_waitcnt lgkmcnt(7)
	v_mfma_f32_16x16x32_bf16 v[62:65], v[142:145], v[190:193], v[62:65]
	v_mfma_f32_16x16x32_bf16 v[58:61], v[150:153], v[190:193], v[58:61]
	s_waitcnt lgkmcnt(5)
	v_mfma_f32_16x16x32_bf16 v[46:49], v[142:145], v[198:201], v[46:49]
	v_mfma_f32_16x16x32_bf16 v[42:45], v[150:153], v[198:201], v[42:45]
	s_waitcnt lgkmcnt(3)
	v_mfma_f32_16x16x32_bf16 v[30:33], v[142:145], v[206:209], v[30:33]
	v_mfma_f32_16x16x32_bf16 v[26:29], v[150:153], v[206:209], v[26:29]
	s_waitcnt lgkmcnt(1)
	v_mfma_f32_16x16x32_bf16 v[14:17], v[142:145], v[214:217], v[14:17]
	v_mfma_f32_16x16x32_bf16 v[10:13], v[150:153], v[214:217], v[10:13]
	v_mfma_f32_16x16x32_bf16 v[62:65], v[146:149], v[194:197], v[62:65]
	v_mfma_f32_16x16x32_bf16 v[58:61], v[170:173], v[194:197], v[58:61]
	v_mfma_f32_16x16x32_bf16 v[46:49], v[146:149], v[202:205], v[46:49]
	v_mfma_f32_16x16x32_bf16 v[42:45], v[170:173], v[202:205], v[42:45]
	v_mfma_f32_16x16x32_bf16 v[30:33], v[146:149], v[210:213], v[30:33]
	v_mfma_f32_16x16x32_bf16 v[26:29], v[170:173], v[210:213], v[26:29]
	s_waitcnt lgkmcnt(0)
	v_mfma_f32_16x16x32_bf16 v[14:17], v[146:149], v[218:221], v[14:17]
	v_mfma_f32_16x16x32_bf16 v[10:13], v[170:173], v[218:221], v[10:13]
	s_setprio 0
	s_setprio 1
	v_mfma_f32_16x16x32_bf16 v[54:57], v[174:177], v[190:193], v[54:57]
	v_mfma_f32_16x16x32_bf16 v[50:53], v[182:185], v[190:193], v[50:53]
	v_mfma_f32_16x16x32_bf16 v[38:41], v[174:177], v[198:201], v[38:41]
	v_mfma_f32_16x16x32_bf16 v[34:37], v[182:185], v[198:201], v[34:37]
	v_mfma_f32_16x16x32_bf16 v[22:25], v[174:177], v[206:209], v[22:25]
	v_mfma_f32_16x16x32_bf16 v[18:21], v[182:185], v[206:209], v[18:21]
	v_mfma_f32_16x16x32_bf16 v[6:9], v[174:177], v[214:217], v[6:9]
	v_mfma_f32_16x16x32_bf16 v[2:5], v[182:185], v[214:217], v[2:5]
	v_mfma_f32_16x16x32_bf16 v[54:57], v[178:181], v[194:197], v[54:57]
	v_mfma_f32_16x16x32_bf16 v[50:53], v[186:189], v[194:197], v[50:53]
	v_mfma_f32_16x16x32_bf16 v[38:41], v[178:181], v[202:205], v[38:41]
	v_mfma_f32_16x16x32_bf16 v[34:37], v[186:189], v[202:205], v[34:37]
	v_mfma_f32_16x16x32_bf16 v[22:25], v[178:181], v[210:213], v[22:25]
	v_mfma_f32_16x16x32_bf16 v[18:21], v[186:189], v[210:213], v[18:21]
	v_mfma_f32_16x16x32_bf16 v[6:9], v[178:181], v[218:221], v[6:9]
	v_mfma_f32_16x16x32_bf16 v[2:5], v[186:189], v[218:221], v[2:5]
	s_setprio 0
	s_barrier
	ds_read_b128 v[142:145], v166
	ds_read_b128 v[146:149], v166 offset:1024
	ds_read_b128 v[150:153], v166 offset:2048
	ds_read_b128 v[170:173], v166 offset:3072
	ds_read_b128 v[174:177], v167
	ds_read_b128 v[178:181], v167 offset:1024
	ds_read_b128 v[182:185], v167 offset:2048
	ds_read_b128 v[186:189], v167 offset:3072
	ds_read_b128 v[190:193], v165 offset:32768
	ds_read_b128 v[194:197], v165 offset:33792
	ds_read_b128 v[198:201], v165 offset:34816
	ds_read_b128 v[202:205], v165 offset:35840
	ds_read_b128 v[206:209], v165 offset:36864
	ds_read_b128 v[210:213], v165 offset:37888
	ds_read_b128 v[214:217], v165 offset:38912
	ds_read_b128 v[218:221], v165 offset:39936
	s_mov_b32 s80, m0
	s_mov_b32 m0, s60
	s_nop 0
	global_load_lds_dwordx4 v159, s[56:57]
	s_mov_b32 m0, s80
	s_nop 0
	s_mov_b32 s80, m0
	s_mov_b32 m0, s61
	s_nop 0
	global_load_lds_dwordx4 v160, s[56:57]
	s_mov_b32 m0, s80
	s_waitcnt vmcnt(8)
	s_waitcnt lgkmcnt(0)
	s_barrier
	s_setprio 1
	s_waitcnt lgkmcnt(7)
	v_mfma_f32_16x16x32_bf16 v[126:129], v[142:145], v[190:193], v[126:129]
	v_mfma_f32_16x16x32_bf16 v[122:125], v[150:153], v[190:193], v[122:125]
	s_waitcnt lgkmcnt(5)
	v_mfma_f32_16x16x32_bf16 v[110:113], v[142:145], v[198:201], v[110:113]
	v_mfma_f32_16x16x32_bf16 v[106:109], v[150:153], v[198:201], v[106:109]
	s_waitcnt lgkmcnt(3)
	v_mfma_f32_16x16x32_bf16 v[94:97], v[142:145], v[206:209], v[94:97]
	v_mfma_f32_16x16x32_bf16 v[90:93], v[150:153], v[206:209], v[90:93]
	s_waitcnt lgkmcnt(1)
	v_mfma_f32_16x16x32_bf16 v[78:81], v[142:145], v[214:217], v[78:81]
	v_mfma_f32_16x16x32_bf16 v[74:77], v[150:153], v[214:217], v[74:77]
	v_mfma_f32_16x16x32_bf16 v[126:129], v[146:149], v[194:197], v[126:129]
	v_mfma_f32_16x16x32_bf16 v[122:125], v[170:173], v[194:197], v[122:125]
	v_mfma_f32_16x16x32_bf16 v[110:113], v[146:149], v[202:205], v[110:113]
	v_mfma_f32_16x16x32_bf16 v[106:109], v[170:173], v[202:205], v[106:109]
	v_mfma_f32_16x16x32_bf16 v[94:97], v[146:149], v[210:213], v[94:97]
	v_mfma_f32_16x16x32_bf16 v[90:93], v[170:173], v[210:213], v[90:93]
	s_waitcnt lgkmcnt(0)
	v_mfma_f32_16x16x32_bf16 v[78:81], v[146:149], v[218:221], v[78:81]
	v_mfma_f32_16x16x32_bf16 v[74:77], v[170:173], v[218:221], v[74:77]
	s_setprio 0
	s_setprio 1
	v_mfma_f32_16x16x32_bf16 v[118:121], v[174:177], v[190:193], v[118:121]
	v_mfma_f32_16x16x32_bf16 v[114:117], v[182:185], v[190:193], v[114:117]
	v_mfma_f32_16x16x32_bf16 v[102:105], v[174:177], v[198:201], v[102:105]
	v_mfma_f32_16x16x32_bf16 v[98:101], v[182:185], v[198:201], v[98:101]
	v_mfma_f32_16x16x32_bf16 v[86:89], v[174:177], v[206:209], v[86:89]
	v_mfma_f32_16x16x32_bf16 v[82:85], v[182:185], v[206:209], v[82:85]
	v_mfma_f32_16x16x32_bf16 v[70:73], v[174:177], v[214:217], v[70:73]
	v_mfma_f32_16x16x32_bf16 v[66:69], v[182:185], v[214:217], v[66:69]
	v_mfma_f32_16x16x32_bf16 v[118:121], v[178:181], v[194:197], v[118:121]
	v_mfma_f32_16x16x32_bf16 v[114:117], v[186:189], v[194:197], v[114:117]
	v_mfma_f32_16x16x32_bf16 v[102:105], v[178:181], v[202:205], v[102:105]
	v_mfma_f32_16x16x32_bf16 v[98:101], v[186:189], v[202:205], v[98:101]
	v_mfma_f32_16x16x32_bf16 v[86:89], v[178:181], v[210:213], v[86:89]
	v_mfma_f32_16x16x32_bf16 v[82:85], v[186:189], v[210:213], v[82:85]
	v_mfma_f32_16x16x32_bf16 v[70:73], v[178:181], v[218:221], v[70:73]
	v_mfma_f32_16x16x32_bf16 v[66:69], v[186:189], v[218:221], v[66:69]
	s_setprio 0
	s_barrier
; #define PG8_STAGEB(bufoff, gbase) PG8_STAGE2(bufoff, gbase, voffB[0], voffB[1])
; #define PG8_STAGEAS(bufoff, gbase, h) PG8_STAGE2(bufoff, gbase, voffA[h][0], voffA[h][1])
; #define PG8_LDA(dst, b, h) do { _Pragma("unroll") for (int m = 0; m < 4; ++m) _Pragma("unroll") for (int k = 0; k < 2; ++k) dst[m][k] = *(const LAS bf16x8*)(lds + PG8_SA(b, h) + aoff + m * 2048 + k * 1024); } while (0)
; #define PG8_WAIT_K() do { if constexpr (HM) PG8_WAIT_V(6); else PG8_WAIT_V(8); } while (0)
; #define PG8_WAIT_L(n) asm volatile("s_waitcnt lgkmcnt(" #n ")" ::: "memory")
; #define PG8_BAR __builtin_amdgcn_s_barrier()
; #define PG8_SCHED __builtin_amdgcn_sched_barrier(0)
;     ...
;             if constexpr (!HM) PG8_LDA(At, 1, 1);
;             PG8_STAGEB(PG8_SB(1, 0), b3); PG8_STAGEB(PG8_SB(1, 1), b3 + hstepB); PG8_STAGEAS(PG8_SA(1, 0), a3, 0);
;             PG8_WAIT_K(); PG8_WAIT_L(0); PG8_BAR; if constexpr (!HM) { PG8_MMA(1, 0, At, B0); PG8_MMA(1, 1, At, B1); } PG8_BAR; PG8_SCHED;
;         }
	ds_read_b128 v[190:193], v165 offset:49152
	ds_read_b128 v[194:197], v165 offset:50176
	s_add_u32 s56, s54, 0x80
	s_addc_u32 s57, s55, 0
	s_mov_b32 s80, m0
	s_mov_b32 m0, s66
	s_nop 0
	global_load_lds_dwordx4 v1, s[56:57]
	s_mov_b32 m0, s80
	ds_read_b128 v[198:201], v165 offset:51200
	ds_read_b128 v[202:205], v165 offset:52224
	s_add_u32 s54, s54, 0x80080
	s_mov_b32 s80, m0
	s_mov_b32 m0, s67
	s_nop 0
	global_load_lds_dwordx4 v156, s[56:57]
	s_mov_b32 m0, s80
	ds_read_b128 v[206:209], v165 offset:53248
	ds_read_b128 v[210:213], v165 offset:54272
	s_addc_u32 s55, s55, 0
	s_mov_b32 s56, m0
	s_mov_b32 m0, s70
	s_nop 0
	global_load_lds_dwordx4 v1, s[54:55]
	s_mov_b32 m0, s56
	ds_read_b128 v[214:217], v165 offset:55296
	ds_read_b128 v[218:221], v165 offset:56320
	s_nop 0
	s_mov_b32 s56, m0
	s_mov_b32 m0, s71
	s_nop 0
	global_load_lds_dwordx4 v156, s[54:55]
	s_mov_b32 m0, s56
	s_mov_b32 s54, m0
	s_mov_b32 m0, s68
	s_nop 0
	global_load_lds_dwordx4 v157, s[12:13]
	s_mov_b32 m0, s54
	s_nop 0
	s_mov_b32 s54, m0
	s_mov_b32 m0, s69
	s_nop 0
	global_load_lds_dwordx4 v158, s[12:13]
	s_mov_b32 m0, s54
	s_waitcnt vmcnt(8)
	s_waitcnt lgkmcnt(0)
	s_barrier
	s_setprio 1
	s_waitcnt lgkmcnt(7)
	v_mfma_f32_16x16x32_bf16 v[62:65], v[142:145], v[190:193], v[62:65]
	v_mfma_f32_16x16x32_bf16 v[58:61], v[150:153], v[190:193], v[58:61]
	s_waitcnt lgkmcnt(5)
	v_mfma_f32_16x16x32_bf16 v[46:49], v[142:145], v[198:201], v[46:49]
	v_mfma_f32_16x16x32_bf16 v[42:45], v[150:153], v[198:201], v[42:45]
	s_waitcnt lgkmcnt(3)
	v_mfma_f32_16x16x32_bf16 v[30:33], v[142:145], v[206:209], v[30:33]
	v_mfma_f32_16x16x32_bf16 v[26:29], v[150:153], v[206:209], v[26:29]
	s_waitcnt lgkmcnt(1)
	v_mfma_f32_16x16x32_bf16 v[14:17], v[142:145], v[214:217], v[14:17]
	v_mfma_f32_16x16x32_bf16 v[10:13], v[150:153], v[214:217], v[10:13]
	v_mfma_f32_16x16x32_bf16 v[62:65], v[146:149], v[194:197], v[62:65]
	v_mfma_f32_16x16x32_bf16 v[58:61], v[170:173], v[194:197], v[58:61]
	v_mfma_f32_16x16x32_bf16 v[46:49], v[146:149], v[202:205], v[46:49]
	v_mfma_f32_16x16x32_bf16 v[42:45], v[170:173], v[202:205], v[42:45]
	v_mfma_f32_16x16x32_bf16 v[30:33], v[146:149], v[210:213], v[30:33]
	v_mfma_f32_16x16x32_bf16 v[26:29], v[170:173], v[210:213], v[26:29]
	s_waitcnt lgkmcnt(0)
	v_mfma_f32_16x16x32_bf16 v[14:17], v[146:149], v[218:221], v[14:17]
	v_mfma_f32_16x16x32_bf16 v[10:13], v[170:173], v[218:221], v[10:13]
	s_setprio 0
	s_setprio 1
	v_mfma_f32_16x16x32_bf16 v[54:57], v[174:177], v[190:193], v[54:57]
	v_mfma_f32_16x16x32_bf16 v[50:53], v[182:185], v[190:193], v[50:53]
	v_mfma_f32_16x16x32_bf16 v[38:41], v[174:177], v[198:201], v[38:41]
	v_mfma_f32_16x16x32_bf16 v[34:37], v[182:185], v[198:201], v[34:37]
	v_mfma_f32_16x16x32_bf16 v[22:25], v[174:177], v[206:209], v[22:25]
	v_mfma_f32_16x16x32_bf16 v[18:21], v[182:185], v[206:209], v[18:21]
	v_mfma_f32_16x16x32_bf16 v[6:9], v[174:177], v[214:217], v[6:9]
	v_mfma_f32_16x16x32_bf16 v[2:5], v[182:185], v[214:217], v[2:5]
	v_mfma_f32_16x16x32_bf16 v[54:57], v[178:181], v[194:197], v[54:57]
	v_mfma_f32_16x16x32_bf16 v[50:53], v[186:189], v[194:197], v[50:53]
	v_mfma_f32_16x16x32_bf16 v[38:41], v[178:181], v[202:205], v[38:41]
	v_mfma_f32_16x16x32_bf16 v[34:37], v[186:189], v[202:205], v[34:37]
	v_mfma_f32_16x16x32_bf16 v[22:25], v[178:181], v[210:213], v[22:25]
	v_mfma_f32_16x16x32_bf16 v[18:21], v[186:189], v[210:213], v[18:21]
	v_mfma_f32_16x16x32_bf16 v[6:9], v[178:181], v[218:221], v[6:9]
	v_mfma_f32_16x16x32_bf16 v[2:5], v[186:189], v[218:221], v[2:5]
	s_setprio 0
	s_barrier
	s_add_i32 s47, s47, 2
	s_add_u32 s4, s4, 0x100
	s_addc_u32 s11, s11, 0
	s_add_u32 s33, s33, 0x100
	s_addc_u32 s45, s45, 0
	s_add_u32 s0, s0, 0x100
	s_addc_u32 s1, s1, 0
	s_cmp_gt_u32 s47, 29
	s_cbranch_scc0 .LBB0_140
	s_and_b64 vcc, exec, s[20:21]
	s_cbranch_vccnz .LBB0_144
	v_lshl_add_u32 v142, s10, 8, v161
	s_cmp_gt_i32 s52, 7
	s_mov_b64 s[0:1], -1
	s_cbranch_scc1 .LBB0_145

; #define LAS __attribute__((address_space(3)))
; #define PG8_STAGEB(bufoff, gbase) PG8_STAGE2(bufoff, gbase, voffB[0], voffB[1])
; #define PG8_STAGEA(bufoff, gbase, h) PG8_STAGE2(bufoff, gbase, voffA[h][0], voffA[h][1])
; #define PG8_STAGEAS(bufoff, gbase, h) PG8_STAGE2(bufoff, gbase, voffA[h][0], voffA[h][1])
; #define PG8_LDA(dst, b, h) do { _Pragma("unroll") for (int m = 0; m < 4; ++m) _Pragma("unroll") for (int k = 0; k < 2; ++k) dst[m][k] = *(const LAS bf16x8*)(lds + PG8_SA(b, h) + aoff + m * 2048 + k * 1024); } while (0)
; #define PG8_LDB(dst, b, h) do { _Pragma("unroll") for (int n = 0; n < 2; ++n) _Pragma("unroll") for (int k = 0; k < 2; ++k) dst[n][k] = *(const LAS bf16x8*)(lds + PG8_SB(b, h) + boff + n * 2048 + k * 1024); } while (0)
; #define PG8_WAIT_K0() do { if (EST > 0 && t == 0 && ui > 0) asm volatile("s_waitcnt vmcnt(%0)" :: "n"((HM ? 6 : 8) + EST) : "memory"); else PG8_WAIT_K(); } while (0)
; #define PG8_WAIT_L(n) asm volatile("s_waitcnt lgkmcnt(" #n ")" ::: "memory")
; #define PG8_BAR __builtin_amdgcn_s_barrier()
; #define PG8_SCHED __builtin_amdgcn_sched_barrier(0)
;     ...
;             PG8_LDB(B0, 0, 0); PG8_LDB(B1, 0, 1); PG8_SCHED; PG8_LDA(At, 0, 0); if constexpr (!HM) PG8_STAGEA(PG8_SA(1, 1), a1, 1);
;             if constexpr (Sched::kGather) { if (last && has_next) { const u32x4 tn = *(const LAS u32x4*)(S.aux + tid * 16); voffA[0][0] = tn.x; voffA[0][1] = tn.y; voffA[1][0] = tn.z; voffA[1][1] = tn.w; } }
;             PG8_WAIT_K0(); PG8_WAIT_L(0); PG8_BAR; PG8_MMA(0, 0, At, B0); PG8_MMA(0, 1, At, B1); PG8_BAR; PG8_SCHED;
;             if constexpr (!HM) PG8_LDA(At, 0, 1);
;             PG8_STAGEB(PG8_SB(0, 0), b2); PG8_STAGEB(PG8_SB(0, 1), b2 + hstepB); PG8_STAGEAS(PG8_SA(0, 0), a2, 0);
;             PG8_WAIT_K0(); PG8_WAIT_L(0); PG8_BAR; if constexpr (!HM) { PG8_MMA(1, 0, At, B0); PG8_MMA(1, 1, At, B1); } PG8_BAR; PG8_SCHED;
.LBB0_581:
	ds_read_b128 v[130:133], v167
	ds_read_b128 v[134:137], v167 offset:1024
	ds_read_b128 v[138:141], v167 offset:2048
	ds_read_b128 v[150:153], v167 offset:3072
	ds_read_b128 v[154:157], v168
	ds_read_b128 v[170:173], v168 offset:1024
	ds_read_b128 v[174:177], v168 offset:2048
	ds_read_b128 v[178:181], v168 offset:3072
	s_cmp_eq_u32 s74, 12
	s_cselect_b32 s46, s0, s29
	s_cselect_b32 s47, s1, s31
	s_cselect_b32 s40, s34, s72
	s_cselect_b32 s41, s35, s73
	s_add_u32 s38, s46, 0x80
	s_addc_u32 s39, s47, 0
	ds_read_b128 v[182:185], v169
	ds_read_b128 v[186:189], v169 offset:1024
	ds_read_b128 v[190:193], v169 offset:2048
	ds_read_b128 v[194:197], v169 offset:3072
	ds_read_b128 v[198:201], v169 offset:4096
	ds_read_b128 v[202:205], v169 offset:5120
	ds_read_b128 v[206:209], v169 offset:6144
	ds_read_b128 v[210:213], v169 offset:7168
	s_mov_b32 s75, m0
	s_mov_b32 m0, s68
	s_nop 0
	global_load_lds_dwordx4 v162, s[42:43]
	s_mov_b32 m0, s75
	s_add_u32 s44, s40, 0x80
	s_mov_b32 s75, m0
	s_mov_b32 m0, s69
	s_nop 0
	global_load_lds_dwordx4 v163, s[42:43]
	s_mov_b32 m0, s75
	s_waitcnt vmcnt(8)
	s_waitcnt lgkmcnt(0)
	s_addc_u32 s45, s41, 0
	s_barrier
	s_setprio 1
	s_waitcnt lgkmcnt(7)
	v_mfma_f32_16x16x32_bf16 v[114:117], v[130:133], v[182:185], v[114:117]
	v_mfma_f32_16x16x32_bf16 v[110:113], v[138:141], v[182:185], v[110:113]
	s_waitcnt lgkmcnt(5)
	v_mfma_f32_16x16x32_bf16 v[106:109], v[130:133], v[190:193], v[106:109]
	v_mfma_f32_16x16x32_bf16 v[102:105], v[138:141], v[190:193], v[102:105]
	s_waitcnt lgkmcnt(3)
	v_mfma_f32_16x16x32_bf16 v[94:97], v[130:133], v[198:201], v[94:97]
	v_mfma_f32_16x16x32_bf16 v[86:89], v[138:141], v[198:201], v[86:89]
	s_waitcnt lgkmcnt(1)
	v_mfma_f32_16x16x32_bf16 v[70:73], v[130:133], v[206:209], v[70:73]
	v_mfma_f32_16x16x32_bf16 v[58:61], v[138:141], v[206:209], v[58:61]
	v_mfma_f32_16x16x32_bf16 v[114:117], v[134:137], v[186:189], v[114:117]
	v_mfma_f32_16x16x32_bf16 v[110:113], v[150:153], v[186:189], v[110:113]
	v_mfma_f32_16x16x32_bf16 v[106:109], v[134:137], v[194:197], v[106:109]
	v_mfma_f32_16x16x32_bf16 v[102:105], v[150:153], v[194:197], v[102:105]
	v_mfma_f32_16x16x32_bf16 v[94:97], v[134:137], v[202:205], v[94:97]
	v_mfma_f32_16x16x32_bf16 v[86:89], v[150:153], v[202:205], v[86:89]
	s_waitcnt lgkmcnt(0)
	v_mfma_f32_16x16x32_bf16 v[70:73], v[134:137], v[210:213], v[70:73]
	v_mfma_f32_16x16x32_bf16 v[58:61], v[150:153], v[210:213], v[58:61]
	s_setprio 0
	s_setprio 1
	v_mfma_f32_16x16x32_bf16 v[126:129], v[154:157], v[182:185], v[126:129]
	v_mfma_f32_16x16x32_bf16 v[122:125], v[174:177], v[182:185], v[122:125]
	v_mfma_f32_16x16x32_bf16 v[118:121], v[154:157], v[190:193], v[118:121]
	v_mfma_f32_16x16x32_bf16 v[98:101], v[174:177], v[190:193], v[98:101]
	v_mfma_f32_16x16x32_bf16 v[90:93], v[154:157], v[198:201], v[90:93]
	v_mfma_f32_16x16x32_bf16 v[82:85], v[174:177], v[198:201], v[82:85]
	v_mfma_f32_16x16x32_bf16 v[66:69], v[154:157], v[206:209], v[66:69]
	v_mfma_f32_16x16x32_bf16 v[54:57], v[174:177], v[206:209], v[54:57]
	v_mfma_f32_16x16x32_bf16 v[126:129], v[170:173], v[186:189], v[126:129]
	v_mfma_f32_16x16x32_bf16 v[122:125], v[178:181], v[186:189], v[122:125]
	v_mfma_f32_16x16x32_bf16 v[118:121], v[170:173], v[194:197], v[118:121]
	v_mfma_f32_16x16x32_bf16 v[98:101], v[178:181], v[194:197], v[98:101]
	v_mfma_f32_16x16x32_bf16 v[90:93], v[170:173], v[202:205], v[90:93]
	v_mfma_f32_16x16x32_bf16 v[82:85], v[178:181], v[202:205], v[82:85]
	v_mfma_f32_16x16x32_bf16 v[66:69], v[170:173], v[210:213], v[66:69]
	v_mfma_f32_16x16x32_bf16 v[54:57], v[178:181], v[210:213], v[54:57]
	s_setprio 0
	s_barrier
	ds_read_b128 v[182:185], v169 offset:16384
	ds_read_b128 v[186:189], v169 offset:17408
	s_mov_b32 s75, m0
	s_mov_b32 m0, s37
	s_nop 0
	global_load_lds_dwordx4 v158, s[40:41]
	s_mov_b32 m0, s75
	ds_read_b128 v[190:193], v169 offset:18432
	ds_read_b128 v[194:197], v169 offset:19456
	s_add_u32 s76, s40, 0x40000
	s_mov_b32 s75, m0
	s_mov_b32 m0, s56
	s_nop 0
	global_load_lds_dwordx4 v159, s[40:41]
	s_mov_b32 m0, s75
	ds_read_b128 v[198:201], v169 offset:20480
	ds_read_b128 v[202:205], v169 offset:21504
	s_addc_u32 s77, s41, 0
	s_mov_b32 s75, m0
	s_mov_b32 m0, s57
	s_nop 0
	global_load_lds_dwordx4 v158, s[76:77]
	s_mov_b32 m0, s75
	ds_read_b128 v[206:209], v169 offset:22528
	ds_read_b128 v[210:213], v169 offset:23552
	s_nop 0
	s_mov_b32 s75, m0
	s_mov_b32 m0, s58
	s_nop 0
	global_load_lds_dwordx4 v159, s[76:77]
	s_mov_b32 m0, s75
	s_nop 0
	s_mov_b32 s75, m0
	s_mov_b32 m0, s55
	s_nop 0
	global_load_lds_dwordx4 v160, s[46:47]
	s_mov_b32 m0, s75
	s_nop 0
	s_mov_b32 s75, m0
	s_mov_b32 m0, s59
	s_nop 0
	global_load_lds_dwordx4 v161, s[46:47]
	s_mov_b32 m0, s75
	s_waitcnt vmcnt(8)
	s_waitcnt lgkmcnt(0)
	s_barrier
; #define PG8_STAGEAS(bufoff, gbase, h) PG8_STAGE2(bufoff, gbase, voffA[h][0], voffA[h][1])
; #define PG8_LDA(dst, b, h) do { _Pragma("unroll") for (int m = 0; m < 4; ++m) _Pragma("unroll") for (int k = 0; k < 2; ++k) dst[m][k] = *(const LAS bf16x8*)(lds + PG8_SA(b, h) + aoff + m * 2048 + k * 1024); } while (0)
; #define PG8_LDB(dst, b, h) do { _Pragma("unroll") for (int n = 0; n < 2; ++n) _Pragma("unroll") for (int k = 0; k < 2; ++k) dst[n][k] = *(const LAS bf16x8*)(lds + PG8_SB(b, h) + boff + n * 2048 + k * 1024); } while (0)
; #define PG8_WAIT_K() do { if constexpr (HM) PG8_WAIT_V(6); else PG8_WAIT_V(8); } while (0)
; #define PG8_WAIT_K0() do { if (EST > 0 && t == 0 && ui > 0) asm volatile("s_waitcnt vmcnt(%0)" :: "n"((HM ? 6 : 8) + EST) : "memory"); else PG8_WAIT_K(); } while (0)
; #define PG8_WAIT_L(n) asm volatile("s_waitcnt lgkmcnt(" #n ")" ::: "memory")
; #define PG8_BAR __builtin_amdgcn_s_barrier()
; #define PG8_SCHED __builtin_amdgcn_sched_barrier(0)
;     ...
;             PG8_WAIT_K0(); PG8_WAIT_L(0); PG8_BAR; if constexpr (!HM) { PG8_MMA(1, 0, At, B0); PG8_MMA(1, 1, At, B1); } PG8_BAR; PG8_SCHED;
;             PG8_LDB(B0, 1, 0); PG8_LDB(B1, 1, 1); PG8_SCHED; PG8_LDA(At, 1, 0); if constexpr (!HM) PG8_STAGEAS(PG8_SA(0, 1), a2, 1);
;             PG8_WAIT_K(); PG8_WAIT_L(0); PG8_BAR; PG8_MMA(0, 0, At, B0); PG8_MMA(0, 1, At, B1); PG8_BAR; PG8_SCHED;
	s_setprio 1
	s_waitcnt lgkmcnt(7)
	v_mfma_f32_16x16x32_bf16 v[78:81], v[130:133], v[182:185], v[78:81]
	v_mfma_f32_16x16x32_bf16 v[74:77], v[138:141], v[182:185], v[74:77]
	s_waitcnt lgkmcnt(5)
	v_mfma_f32_16x16x32_bf16 v[46:49], v[130:133], v[190:193], v[46:49]
	v_mfma_f32_16x16x32_bf16 v[42:45], v[138:141], v[190:193], v[42:45]
	s_waitcnt lgkmcnt(3)
	v_mfma_f32_16x16x32_bf16 v[30:33], v[130:133], v[198:201], v[30:33]
	v_mfma_f32_16x16x32_bf16 v[26:29], v[138:141], v[198:201], v[26:29]
	s_waitcnt lgkmcnt(1)
	v_mfma_f32_16x16x32_bf16 v[14:17], v[130:133], v[206:209], v[14:17]
	v_mfma_f32_16x16x32_bf16 v[10:13], v[138:141], v[206:209], v[10:13]
	v_mfma_f32_16x16x32_bf16 v[78:81], v[134:137], v[186:189], v[78:81]
	v_mfma_f32_16x16x32_bf16 v[74:77], v[150:153], v[186:189], v[74:77]
	v_mfma_f32_16x16x32_bf16 v[46:49], v[134:137], v[194:197], v[46:49]
	v_mfma_f32_16x16x32_bf16 v[42:45], v[150:153], v[194:197], v[42:45]
	v_mfma_f32_16x16x32_bf16 v[30:33], v[134:137], v[202:205], v[30:33]
	v_mfma_f32_16x16x32_bf16 v[26:29], v[150:153], v[202:205], v[26:29]
	s_waitcnt lgkmcnt(0)
	v_mfma_f32_16x16x32_bf16 v[14:17], v[134:137], v[210:213], v[14:17]
	v_mfma_f32_16x16x32_bf16 v[10:13], v[150:153], v[210:213], v[10:13]
	s_setprio 0
	s_setprio 1
	v_mfma_f32_16x16x32_bf16 v[62:65], v[154:157], v[182:185], v[62:65]
	v_mfma_f32_16x16x32_bf16 v[50:53], v[174:177], v[182:185], v[50:53]
	v_mfma_f32_16x16x32_bf16 v[38:41], v[154:157], v[190:193], v[38:41]
	v_mfma_f32_16x16x32_bf16 v[34:37], v[174:177], v[190:193], v[34:37]
	v_mfma_f32_16x16x32_bf16 v[22:25], v[154:157], v[198:201], v[22:25]
	v_mfma_f32_16x16x32_bf16 v[18:21], v[174:177], v[198:201], v[18:21]
	v_mfma_f32_16x16x32_bf16 v[6:9], v[154:157], v[206:209], v[6:9]
	v_mfma_f32_16x16x32_bf16 v[2:5], v[174:177], v[206:209], v[2:5]
	v_mfma_f32_16x16x32_bf16 v[62:65], v[170:173], v[186:189], v[62:65]
	v_mfma_f32_16x16x32_bf16 v[50:53], v[178:181], v[186:189], v[50:53]
	v_mfma_f32_16x16x32_bf16 v[38:41], v[170:173], v[194:197], v[38:41]
	v_mfma_f32_16x16x32_bf16 v[34:37], v[178:181], v[194:197], v[34:37]
	v_mfma_f32_16x16x32_bf16 v[22:25], v[170:173], v[202:205], v[22:25]
	v_mfma_f32_16x16x32_bf16 v[18:21], v[178:181], v[202:205], v[18:21]
	v_mfma_f32_16x16x32_bf16 v[6:9], v[170:173], v[210:213], v[6:9]
	v_mfma_f32_16x16x32_bf16 v[2:5], v[178:181], v[210:213], v[2:5]
	s_setprio 0
	s_barrier
	ds_read_b128 v[130:133], v142
	ds_read_b128 v[134:137], v142 offset:1024
	ds_read_b128 v[138:141], v142 offset:2048
	ds_read_b128 v[150:153], v142 offset:3072
	ds_read_b128 v[154:157], v143
	ds_read_b128 v[170:173], v143 offset:1024
	ds_read_b128 v[174:177], v143 offset:2048
	ds_read_b128 v[178:181], v143 offset:3072
	ds_read_b128 v[182:185], v169 offset:32768
	ds_read_b128 v[186:189], v169 offset:33792
	ds_read_b128 v[190:193], v169 offset:34816
	ds_read_b128 v[194:197], v169 offset:35840
	ds_read_b128 v[198:201], v169 offset:36864
	ds_read_b128 v[202:205], v169 offset:37888
	ds_read_b128 v[206:209], v169 offset:38912
	ds_read_b128 v[210:213], v169 offset:39936
	s_mov_b32 s75, m0
	s_mov_b32 m0, s60
	s_nop 0
	global_load_lds_dwordx4 v162, s[46:47]
	s_mov_b32 m0, s75
	s_nop 0
	s_mov_b32 s75, m0
	s_mov_b32 m0, s61
	s_nop 0
	global_load_lds_dwordx4 v163, s[46:47]
	s_mov_b32 m0, s75
	s_waitcnt vmcnt(8)
	s_waitcnt lgkmcnt(0)
	s_barrier
	s_setprio 1
	s_waitcnt lgkmcnt(7)
	v_mfma_f32_16x16x32_bf16 v[114:117], v[130:133], v[182:185], v[114:117]
	v_mfma_f32_16x16x32_bf16 v[110:113], v[138:141], v[182:185], v[110:113]
	s_waitcnt lgkmcnt(5)
	v_mfma_f32_16x16x32_bf16 v[106:109], v[130:133], v[190:193], v[106:109]
	v_mfma_f32_16x16x32_bf16 v[102:105], v[138:141], v[190:193], v[102:105]
	s_waitcnt lgkmcnt(3)
	v_mfma_f32_16x16x32_bf16 v[94:97], v[130:133], v[198:201], v[94:97]
	v_mfma_f32_16x16x32_bf16 v[86:89], v[138:141], v[198:201], v[86:89]
	s_waitcnt lgkmcnt(1)
	v_mfma_f32_16x16x32_bf16 v[70:73], v[130:133], v[206:209], v[70:73]
	v_mfma_f32_16x16x32_bf16 v[58:61], v[138:141], v[206:209], v[58:61]
	v_mfma_f32_16x16x32_bf16 v[114:117], v[134:137], v[186:189], v[114:117]
	v_mfma_f32_16x16x32_bf16 v[110:113], v[150:153], v[186:189], v[110:113]
	v_mfma_f32_16x16x32_bf16 v[106:109], v[134:137], v[194:197], v[106:109]
	v_mfma_f32_16x16x32_bf16 v[102:105], v[150:153], v[194:197], v[102:105]
	v_mfma_f32_16x16x32_bf16 v[94:97], v[134:137], v[202:205], v[94:97]
	v_mfma_f32_16x16x32_bf16 v[86:89], v[150:153], v[202:205], v[86:89]
	s_waitcnt lgkmcnt(0)
	v_mfma_f32_16x16x32_bf16 v[70:73], v[134:137], v[210:213], v[70:73]
	v_mfma_f32_16x16x32_bf16 v[58:61], v[150:153], v[210:213], v[58:61]
	s_setprio 0
	s_setprio 1
	v_mfma_f32_16x16x32_bf16 v[126:129], v[154:157], v[182:185], v[126:129]
	v_mfma_f32_16x16x32_bf16 v[122:125], v[174:177], v[182:185], v[122:125]
	v_mfma_f32_16x16x32_bf16 v[118:121], v[154:157], v[190:193], v[118:121]
	v_mfma_f32_16x16x32_bf16 v[98:101], v[174:177], v[190:193], v[98:101]
	v_mfma_f32_16x16x32_bf16 v[90:93], v[154:157], v[198:201], v[90:93]
	v_mfma_f32_16x16x32_bf16 v[82:85], v[174:177], v[198:201], v[82:85]
	v_mfma_f32_16x16x32_bf16 v[66:69], v[154:157], v[206:209], v[66:69]
	v_mfma_f32_16x16x32_bf16 v[54:57], v[174:177], v[206:209], v[54:57]
	v_mfma_f32_16x16x32_bf16 v[126:129], v[170:173], v[186:189], v[126:129]
	v_mfma_f32_16x16x32_bf16 v[122:125], v[178:181], v[186:189], v[122:125]
	v_mfma_f32_16x16x32_bf16 v[118:121], v[170:173], v[194:197], v[118:121]
	v_mfma_f32_16x16x32_bf16 v[98:101], v[178:181], v[194:197], v[98:101]
	v_mfma_f32_16x16x32_bf16 v[90:93], v[170:173], v[202:205], v[90:93]
	v_mfma_f32_16x16x32_bf16 v[82:85], v[178:181], v[202:205], v[82:85]
	v_mfma_f32_16x16x32_bf16 v[66:69], v[170:173], v[210:213], v[66:69]
	v_mfma_f32_16x16x32_bf16 v[54:57], v[178:181], v[210:213], v[54:57]
	s_setprio 0
	s_barrier
; #define PG8_STAGEB(bufoff, gbase) PG8_STAGE2(bufoff, gbase, voffB[0], voffB[1])
; #define PG8_STAGEAS(bufoff, gbase, h) PG8_STAGE2(bufoff, gbase, voffA[h][0], voffA[h][1])
; #define PG8_LDA(dst, b, h) do { _Pragma("unroll") for (int m = 0; m < 4; ++m) _Pragma("unroll") for (int k = 0; k < 2; ++k) dst[m][k] = *(const LAS bf16x8*)(lds + PG8_SA(b, h) + aoff + m * 2048 + k * 1024); } while (0)
; #define PG8_WAIT_K() do { if constexpr (HM) PG8_WAIT_V(6); else PG8_WAIT_V(8); } while (0)
; #define PG8_WAIT_L(n) asm volatile("s_waitcnt lgkmcnt(" #n ")" ::: "memory")
; #define PG8_BAR __builtin_amdgcn_s_barrier()
; #define PG8_SCHED __builtin_amdgcn_sched_barrier(0)
;     ...
;             if constexpr (!HM) PG8_LDA(At, 1, 1);
;             PG8_STAGEB(PG8_SB(1, 0), b3); PG8_STAGEB(PG8_SB(1, 1), b3 + hstepB); PG8_STAGEAS(PG8_SA(1, 0), a3, 0);
;             PG8_WAIT_K(); PG8_WAIT_L(0); PG8_BAR; if constexpr (!HM) { PG8_MMA(1, 0, At, B0); PG8_MMA(1, 1, At, B1); } PG8_BAR; PG8_SCHED;
;         }
;         if (wr == 0) PG8_BAR;
	ds_read_b128 v[182:185], v169 offset:49152
	ds_read_b128 v[186:189], v169 offset:50176
	s_mov_b32 s46, m0
	s_mov_b32 m0, s62
	s_nop 0
	global_load_lds_dwordx4 v158, s[44:45]
	s_mov_b32 m0, s46
	ds_read_b128 v[190:193], v169 offset:51200
	ds_read_b128 v[194:197], v169 offset:52224
	s_add_u32 s40, s40, 0x40080
	s_mov_b32 s46, m0
	s_mov_b32 m0, s63
	s_nop 0
	global_load_lds_dwordx4 v159, s[44:45]
	s_mov_b32 m0, s46
	ds_read_b128 v[198:201], v169 offset:53248
	ds_read_b128 v[202:205], v169 offset:54272
	s_addc_u32 s41, s41, 0
	s_mov_b32 s44, m0
	s_mov_b32 m0, s66
	s_nop 0
	global_load_lds_dwordx4 v158, s[40:41]
	s_mov_b32 m0, s44
	ds_read_b128 v[206:209], v169 offset:55296
	ds_read_b128 v[210:213], v169 offset:56320
	s_nop 0
	s_mov_b32 s44, m0
	s_mov_b32 m0, s67
	s_nop 0
	global_load_lds_dwordx4 v159, s[40:41]
	s_mov_b32 m0, s44
	s_mov_b32 s40, m0
	s_mov_b32 m0, s64
	s_nop 0
	global_load_lds_dwordx4 v160, s[38:39]
	s_mov_b32 m0, s40
	s_nop 0
	s_mov_b32 s40, m0
	s_mov_b32 m0, s65
	s_nop 0
	global_load_lds_dwordx4 v161, s[38:39]
	s_mov_b32 m0, s40
	s_waitcnt vmcnt(8)
	s_waitcnt lgkmcnt(0)
	s_barrier
	s_setprio 1
	s_waitcnt lgkmcnt(7)
	v_mfma_f32_16x16x32_bf16 v[78:81], v[130:133], v[182:185], v[78:81]
	v_mfma_f32_16x16x32_bf16 v[74:77], v[138:141], v[182:185], v[74:77]
	s_waitcnt lgkmcnt(5)
	v_mfma_f32_16x16x32_bf16 v[46:49], v[130:133], v[190:193], v[46:49]
	v_mfma_f32_16x16x32_bf16 v[42:45], v[138:141], v[190:193], v[42:45]
	s_waitcnt lgkmcnt(3)
	v_mfma_f32_16x16x32_bf16 v[30:33], v[130:133], v[198:201], v[30:33]
	v_mfma_f32_16x16x32_bf16 v[26:29], v[138:141], v[198:201], v[26:29]
	s_waitcnt lgkmcnt(1)
	v_mfma_f32_16x16x32_bf16 v[14:17], v[130:133], v[206:209], v[14:17]
	v_mfma_f32_16x16x32_bf16 v[10:13], v[138:141], v[206:209], v[10:13]
	v_mfma_f32_16x16x32_bf16 v[78:81], v[134:137], v[186:189], v[78:81]
	v_mfma_f32_16x16x32_bf16 v[74:77], v[150:153], v[186:189], v[74:77]
	v_mfma_f32_16x16x32_bf16 v[46:49], v[134:137], v[194:197], v[46:49]
	v_mfma_f32_16x16x32_bf16 v[42:45], v[150:153], v[194:197], v[42:45]
	v_mfma_f32_16x16x32_bf16 v[30:33], v[134:137], v[202:205], v[30:33]
	v_mfma_f32_16x16x32_bf16 v[26:29], v[150:153], v[202:205], v[26:29]
	s_waitcnt lgkmcnt(0)
	v_mfma_f32_16x16x32_bf16 v[14:17], v[134:137], v[210:213], v[14:17]
	v_mfma_f32_16x16x32_bf16 v[10:13], v[150:153], v[210:213], v[10:13]
	s_setprio 0
	s_setprio 1
	v_mfma_f32_16x16x32_bf16 v[62:65], v[154:157], v[182:185], v[62:65]
	v_mfma_f32_16x16x32_bf16 v[50:53], v[174:177], v[182:185], v[50:53]
	v_mfma_f32_16x16x32_bf16 v[38:41], v[154:157], v[190:193], v[38:41]
	v_mfma_f32_16x16x32_bf16 v[34:37], v[174:177], v[190:193], v[34:37]
	v_mfma_f32_16x16x32_bf16 v[22:25], v[154:157], v[198:201], v[22:25]
	v_mfma_f32_16x16x32_bf16 v[18:21], v[174:177], v[198:201], v[18:21]
	v_mfma_f32_16x16x32_bf16 v[6:9], v[154:157], v[206:209], v[6:9]
	v_mfma_f32_16x16x32_bf16 v[2:5], v[174:177], v[206:209], v[2:5]
	v_mfma_f32_16x16x32_bf16 v[62:65], v[170:173], v[186:189], v[62:65]
	v_mfma_f32_16x16x32_bf16 v[50:53], v[178:181], v[186:189], v[50:53]
	v_mfma_f32_16x16x32_bf16 v[38:41], v[170:173], v[194:197], v[38:41]
	v_mfma_f32_16x16x32_bf16 v[34:37], v[178:181], v[194:197], v[34:37]
	v_mfma_f32_16x16x32_bf16 v[22:25], v[170:173], v[202:205], v[22:25]
	v_mfma_f32_16x16x32_bf16 v[18:21], v[178:181], v[202:205], v[18:21]
	v_mfma_f32_16x16x32_bf16 v[6:9], v[170:173], v[210:213], v[6:9]
	v_mfma_f32_16x16x32_bf16 v[2:5], v[178:181], v[210:213], v[2:5]
	s_setprio 0
	s_barrier
	s_add_i32 s74, s74, 2
	s_add_u32 s29, s29, 0x100
	s_addc_u32 s31, s31, 0
	s_add_u32 s72, s72, 0x100
	s_addc_u32 s73, s73, 0
	s_add_u32 s42, s42, 0x100
	s_addc_u32 s43, s43, 0
	s_cmp_gt_u32 s74, 13
	s_cbranch_scc0 .LBB0_581
	s_and_b64 vcc, exec, s[18:19]
	s_cbranch_vccz .LBB0_584
	s_barrier

; #define LAS __attribute__((address_space(3)))
; #define PG8_STAGEB(bufoff, gbase) PG8_STAGE2(bufoff, gbase, voffB[0], voffB[1])
; #define PG8_STAGEA(bufoff, gbase, h) PG8_STAGE2(bufoff, gbase, voffA[h][0], voffA[h][1])
; #define PG8_STAGEAS(bufoff, gbase, h) PG8_STAGE2(bufoff, gbase, voffA[h][0], voffA[h][1])
; #define PG8_LDA(dst, b, h) do { _Pragma("unroll") for (int m = 0; m < 4; ++m) _Pragma("unroll") for (int k = 0; k < 2; ++k) dst[m][k] = *(const LAS bf16x8*)(lds + PG8_SA(b, h) + aoff + m * 2048 + k * 1024); } while (0)
; #define PG8_LDB(dst, b, h) do { _Pragma("unroll") for (int n = 0; n < 2; ++n) _Pragma("unroll") for (int k = 0; k < 2; ++k) dst[n][k] = *(const LAS bf16x8*)(lds + PG8_SB(b, h) + boff + n * 2048 + k * 1024); } while (0)
; #define PG8_WAIT_K0() do { if (EST > 0 && t == 0 && ui > 0) asm volatile("s_waitcnt vmcnt(%0)" :: "n"((HM ? 6 : 8) + EST) : "memory"); else PG8_WAIT_K(); } while (0)
; #define PG8_WAIT_L(n) asm volatile("s_waitcnt lgkmcnt(" #n ")" ::: "memory")
; #define PG8_BAR __builtin_amdgcn_s_barrier()
; #define PG8_SCHED __builtin_amdgcn_sched_barrier(0)
;     ...
;             PG8_LDB(B0, 0, 0); PG8_LDB(B1, 0, 1); PG8_SCHED; PG8_LDA(At, 0, 0); if constexpr (!HM) PG8_STAGEA(PG8_SA(1, 1), a1, 1);
;             if constexpr (Sched::kGather) { if (last && has_next) { const u32x4 tn = *(const LAS u32x4*)(S.aux + tid * 16); voffA[0][0] = tn.x; voffA[0][1] = tn.y; voffA[1][0] = tn.z; voffA[1][1] = tn.w; } }
;             PG8_WAIT_K0(); PG8_WAIT_L(0); PG8_BAR; PG8_MMA(0, 0, At, B0); PG8_MMA(0, 1, At, B1); PG8_BAR; PG8_SCHED;
;             if constexpr (!HM) PG8_LDA(At, 0, 1);
;             PG8_STAGEB(PG8_SB(0, 0), b2); PG8_STAGEB(PG8_SB(0, 1), b2 + hstepB); PG8_STAGEAS(PG8_SA(0, 0), a2, 0);
.LBB0_611:
	ds_read_b128 v[130:133], v180
	ds_read_b128 v[134:137], v180 offset:1024
	ds_read_b128 v[138:141], v180 offset:2048
	ds_read_b128 v[142:145], v180 offset:3072
	ds_read_b128 v[148:151], v181
	ds_read_b128 v[152:155], v181 offset:1024
	ds_read_b128 v[156:159], v181 offset:2048
	ds_read_b128 v[162:165], v181 offset:3072
	s_cmp_eq_u32 s59, 28
	s_cselect_b32 s34, s0, s17
	s_cselect_b32 s35, s1, s19
	s_cselect_b32 s26, s20, s57
	s_cselect_b32 s27, s21, s58
	s_add_u32 s24, s34, 0x80
	s_addc_u32 s25, s35, 0
	ds_read_b128 v[166:169], v182
	ds_read_b128 v[184:187], v182 offset:1024
	ds_read_b128 v[188:191], v182 offset:2048
	ds_read_b128 v[192:195], v182 offset:3072
	ds_read_b128 v[196:199], v182 offset:4096
	ds_read_b128 v[200:203], v182 offset:5120
	ds_read_b128 v[204:207], v182 offset:6144
	ds_read_b128 v[208:211], v182 offset:7168
	s_mov_b32 s60, m0
	s_mov_b32 m0, s53
	s_nop 0
	global_load_lds_dwordx4 v175, s[28:29]
	s_mov_b32 m0, s60
	s_add_u32 s30, s26, 0x80
	s_mov_b32 s60, m0
	s_mov_b32 m0, s54
	s_nop 0
	global_load_lds_dwordx4 v176, s[28:29]
	s_mov_b32 m0, s60
	s_waitcnt vmcnt(8)
	s_waitcnt lgkmcnt(0)
	s_addc_u32 s31, s27, 0
	s_barrier
	s_setprio 1
	s_waitcnt lgkmcnt(7)
	v_mfma_f32_16x16x32_bf16 v[126:129], v[130:133], v[166:169], v[126:129]
	v_mfma_f32_16x16x32_bf16 v[122:125], v[138:141], v[166:169], v[122:125]
	s_waitcnt lgkmcnt(5)
	v_mfma_f32_16x16x32_bf16 v[110:113], v[130:133], v[188:191], v[110:113]
	v_mfma_f32_16x16x32_bf16 v[106:109], v[138:141], v[188:191], v[106:109]
	s_waitcnt lgkmcnt(3)
	v_mfma_f32_16x16x32_bf16 v[94:97], v[130:133], v[196:199], v[94:97]
	v_mfma_f32_16x16x32_bf16 v[90:93], v[138:141], v[196:199], v[90:93]
	s_waitcnt lgkmcnt(1)
	v_mfma_f32_16x16x32_bf16 v[78:81], v[130:133], v[204:207], v[78:81]
	v_mfma_f32_16x16x32_bf16 v[74:77], v[138:141], v[204:207], v[74:77]
	v_mfma_f32_16x16x32_bf16 v[126:129], v[134:137], v[184:187], v[126:129]
	v_mfma_f32_16x16x32_bf16 v[122:125], v[142:145], v[184:187], v[122:125]
	v_mfma_f32_16x16x32_bf16 v[110:113], v[134:137], v[192:195], v[110:113]
	v_mfma_f32_16x16x32_bf16 v[106:109], v[142:145], v[192:195], v[106:109]
	v_mfma_f32_16x16x32_bf16 v[94:97], v[134:137], v[200:203], v[94:97]
	v_mfma_f32_16x16x32_bf16 v[90:93], v[142:145], v[200:203], v[90:93]
	s_waitcnt lgkmcnt(0)
	v_mfma_f32_16x16x32_bf16 v[78:81], v[134:137], v[208:211], v[78:81]
	v_mfma_f32_16x16x32_bf16 v[74:77], v[142:145], v[208:211], v[74:77]
	s_setprio 0
	s_setprio 1
	v_mfma_f32_16x16x32_bf16 v[118:121], v[148:151], v[166:169], v[118:121]
	v_mfma_f32_16x16x32_bf16 v[114:117], v[156:159], v[166:169], v[114:117]
	v_mfma_f32_16x16x32_bf16 v[102:105], v[148:151], v[188:191], v[102:105]
	v_mfma_f32_16x16x32_bf16 v[98:101], v[156:159], v[188:191], v[98:101]
	v_mfma_f32_16x16x32_bf16 v[86:89], v[148:151], v[196:199], v[86:89]
	v_mfma_f32_16x16x32_bf16 v[82:85], v[156:159], v[196:199], v[82:85]
	v_mfma_f32_16x16x32_bf16 v[70:73], v[148:151], v[204:207], v[70:73]
	v_mfma_f32_16x16x32_bf16 v[66:69], v[156:159], v[204:207], v[66:69]
	v_mfma_f32_16x16x32_bf16 v[118:121], v[152:155], v[184:187], v[118:121]
	v_mfma_f32_16x16x32_bf16 v[114:117], v[162:165], v[184:187], v[114:117]
	v_mfma_f32_16x16x32_bf16 v[102:105], v[152:155], v[192:195], v[102:105]
	v_mfma_f32_16x16x32_bf16 v[98:101], v[162:165], v[192:195], v[98:101]
	v_mfma_f32_16x16x32_bf16 v[86:89], v[152:155], v[200:203], v[86:89]
	v_mfma_f32_16x16x32_bf16 v[82:85], v[162:165], v[200:203], v[82:85]
	v_mfma_f32_16x16x32_bf16 v[70:73], v[152:155], v[208:211], v[70:73]
	v_mfma_f32_16x16x32_bf16 v[66:69], v[162:165], v[208:211], v[66:69]
	s_setprio 0
	s_barrier
	ds_read_b128 v[166:169], v182 offset:16384
	ds_read_b128 v[184:187], v182 offset:17408
	s_mov_b32 s60, m0
	s_mov_b32 m0, s23
	s_nop 0
	global_load_lds_dwordx4 v1, s[26:27]
	s_mov_b32 m0, s60
	ds_read_b128 v[188:191], v182 offset:18432
	ds_read_b128 v[192:195], v182 offset:19456
	s_nop 0
	s_mov_b32 s60, m0
	s_mov_b32 m0, s41
	s_nop 0
	global_load_lds_dwordx4 v172, s[26:27]
	s_mov_b32 m0, s60
	ds_read_b128 v[196:199], v182 offset:20480
	ds_read_b128 v[200:203], v182 offset:21504
	s_add_u32 s60, s26, 0x80000
	s_addc_u32 s61, s27, 0
	s_mov_b32 s62, m0
	s_mov_b32 m0, s42
	s_nop 0
	global_load_lds_dwordx4 v1, s[60:61]
	s_mov_b32 m0, s62
	ds_read_b128 v[204:207], v182 offset:22528
	ds_read_b128 v[208:211], v182 offset:23552
	s_nop 0
	s_mov_b32 s62, m0
	s_mov_b32 m0, s43
	s_nop 0
	global_load_lds_dwordx4 v172, s[60:61]
	s_mov_b32 m0, s62
	s_mov_b32 s60, m0
	s_mov_b32 m0, s36
	s_nop 0
	global_load_lds_dwordx4 v173, s[34:35]
	s_mov_b32 m0, s60
	s_nop 0
	s_mov_b32 s60, m0
	s_mov_b32 m0, s44
	s_nop 0
	global_load_lds_dwordx4 v174, s[34:35]
	s_mov_b32 m0, s60
	s_waitcnt vmcnt(8)
	s_waitcnt lgkmcnt(0)
	s_barrier
; #define PG8_STAGEAS(bufoff, gbase, h) PG8_STAGE2(bufoff, gbase, voffA[h][0], voffA[h][1])
; #define PG8_LDA(dst, b, h) do { _Pragma("unroll") for (int m = 0; m < 4; ++m) _Pragma("unroll") for (int k = 0; k < 2; ++k) dst[m][k] = *(const LAS bf16x8*)(lds + PG8_SA(b, h) + aoff + m * 2048 + k * 1024); } while (0)
; #define PG8_LDB(dst, b, h) do { _Pragma("unroll") for (int n = 0; n < 2; ++n) _Pragma("unroll") for (int k = 0; k < 2; ++k) dst[n][k] = *(const LAS bf16x8*)(lds + PG8_SB(b, h) + boff + n * 2048 + k * 1024); } while (0)
; #define PG8_WAIT_K() do { if constexpr (HM) PG8_WAIT_V(6); else PG8_WAIT_V(8); } while (0)
; #define PG8_WAIT_K0() do { if (EST > 0 && t == 0 && ui > 0) asm volatile("s_waitcnt vmcnt(%0)" :: "n"((HM ? 6 : 8) + EST) : "memory"); else PG8_WAIT_K(); } while (0)
; #define PG8_WAIT_L(n) asm volatile("s_waitcnt lgkmcnt(" #n ")" ::: "memory")
; #define PG8_BAR __builtin_amdgcn_s_barrier()
; #define PG8_SCHED __builtin_amdgcn_sched_barrier(0)
;     ...
;             PG8_WAIT_K0(); PG8_WAIT_L(0); PG8_BAR; if constexpr (!HM) { PG8_MMA(1, 0, At, B0); PG8_MMA(1, 1, At, B1); } PG8_BAR; PG8_SCHED;
;             PG8_LDB(B0, 1, 0); PG8_LDB(B1, 1, 1); PG8_SCHED; PG8_LDA(At, 1, 0); if constexpr (!HM) PG8_STAGEAS(PG8_SA(0, 1), a2, 1);
;             PG8_WAIT_K(); PG8_WAIT_L(0); PG8_BAR; PG8_MMA(0, 0, At, B0); PG8_MMA(0, 1, At, B1); PG8_BAR; PG8_SCHED;
	s_setprio 1
	s_waitcnt lgkmcnt(7)
	v_mfma_f32_16x16x32_bf16 v[62:65], v[130:133], v[166:169], v[62:65]
	v_mfma_f32_16x16x32_bf16 v[58:61], v[138:141], v[166:169], v[58:61]
	s_waitcnt lgkmcnt(5)
	v_mfma_f32_16x16x32_bf16 v[46:49], v[130:133], v[188:191], v[46:49]
	v_mfma_f32_16x16x32_bf16 v[42:45], v[138:141], v[188:191], v[42:45]
	s_waitcnt lgkmcnt(3)
	v_mfma_f32_16x16x32_bf16 v[30:33], v[130:133], v[196:199], v[30:33]
	v_mfma_f32_16x16x32_bf16 v[26:29], v[138:141], v[196:199], v[26:29]
	s_waitcnt lgkmcnt(1)
	v_mfma_f32_16x16x32_bf16 v[14:17], v[130:133], v[204:207], v[14:17]
	v_mfma_f32_16x16x32_bf16 v[10:13], v[138:141], v[204:207], v[10:13]
	v_mfma_f32_16x16x32_bf16 v[62:65], v[134:137], v[184:187], v[62:65]
	v_mfma_f32_16x16x32_bf16 v[58:61], v[142:145], v[184:187], v[58:61]
	v_mfma_f32_16x16x32_bf16 v[46:49], v[134:137], v[192:195], v[46:49]
	v_mfma_f32_16x16x32_bf16 v[42:45], v[142:145], v[192:195], v[42:45]
	v_mfma_f32_16x16x32_bf16 v[30:33], v[134:137], v[200:203], v[30:33]
	v_mfma_f32_16x16x32_bf16 v[26:29], v[142:145], v[200:203], v[26:29]
	s_waitcnt lgkmcnt(0)
	v_mfma_f32_16x16x32_bf16 v[14:17], v[134:137], v[208:211], v[14:17]
	v_mfma_f32_16x16x32_bf16 v[10:13], v[142:145], v[208:211], v[10:13]
	s_setprio 0
	s_setprio 1
	v_mfma_f32_16x16x32_bf16 v[54:57], v[148:151], v[166:169], v[54:57]
	v_mfma_f32_16x16x32_bf16 v[50:53], v[156:159], v[166:169], v[50:53]
	v_mfma_f32_16x16x32_bf16 v[38:41], v[148:151], v[188:191], v[38:41]
	v_mfma_f32_16x16x32_bf16 v[34:37], v[156:159], v[188:191], v[34:37]
	v_mfma_f32_16x16x32_bf16 v[22:25], v[148:151], v[196:199], v[22:25]
	v_mfma_f32_16x16x32_bf16 v[18:21], v[156:159], v[196:199], v[18:21]
	v_mfma_f32_16x16x32_bf16 v[6:9], v[148:151], v[204:207], v[6:9]
	v_mfma_f32_16x16x32_bf16 v[2:5], v[156:159], v[204:207], v[2:5]
	v_mfma_f32_16x16x32_bf16 v[54:57], v[152:155], v[184:187], v[54:57]
	v_mfma_f32_16x16x32_bf16 v[50:53], v[162:165], v[184:187], v[50:53]
	v_mfma_f32_16x16x32_bf16 v[38:41], v[152:155], v[192:195], v[38:41]
	v_mfma_f32_16x16x32_bf16 v[34:37], v[162:165], v[192:195], v[34:37]
	v_mfma_f32_16x16x32_bf16 v[22:25], v[152:155], v[200:203], v[22:25]
	v_mfma_f32_16x16x32_bf16 v[18:21], v[162:165], v[200:203], v[18:21]
	v_mfma_f32_16x16x32_bf16 v[6:9], v[152:155], v[208:211], v[6:9]
	v_mfma_f32_16x16x32_bf16 v[2:5], v[162:165], v[208:211], v[2:5]
	s_setprio 0
	s_barrier
	ds_read_b128 v[130:133], v146
	ds_read_b128 v[134:137], v146 offset:1024
	ds_read_b128 v[138:141], v146 offset:2048
	ds_read_b128 v[142:145], v146 offset:3072
	ds_read_b128 v[148:151], v147
	ds_read_b128 v[152:155], v147 offset:1024
	ds_read_b128 v[156:159], v147 offset:2048
	ds_read_b128 v[162:165], v147 offset:3072
	ds_read_b128 v[166:169], v182 offset:32768
	ds_read_b128 v[184:187], v182 offset:33792
	ds_read_b128 v[188:191], v182 offset:34816
	ds_read_b128 v[192:195], v182 offset:35840
	ds_read_b128 v[196:199], v182 offset:36864
	ds_read_b128 v[200:203], v182 offset:37888
	ds_read_b128 v[204:207], v182 offset:38912
	ds_read_b128 v[208:211], v182 offset:39936
	s_mov_b32 s60, m0
	s_mov_b32 m0, s45
	s_nop 0
	global_load_lds_dwordx4 v175, s[34:35]
	s_mov_b32 m0, s60
	s_nop 0
	s_mov_b32 s60, m0
	s_mov_b32 m0, s46
	s_nop 0
	global_load_lds_dwordx4 v176, s[34:35]
	s_mov_b32 m0, s60
	s_waitcnt vmcnt(8)
	s_waitcnt lgkmcnt(0)
	s_barrier
	s_setprio 1
	s_waitcnt lgkmcnt(7)
	v_mfma_f32_16x16x32_bf16 v[126:129], v[130:133], v[166:169], v[126:129]
	v_mfma_f32_16x16x32_bf16 v[122:125], v[138:141], v[166:169], v[122:125]
	s_waitcnt lgkmcnt(5)
	v_mfma_f32_16x16x32_bf16 v[110:113], v[130:133], v[188:191], v[110:113]
	v_mfma_f32_16x16x32_bf16 v[106:109], v[138:141], v[188:191], v[106:109]
	s_waitcnt lgkmcnt(3)
	v_mfma_f32_16x16x32_bf16 v[94:97], v[130:133], v[196:199], v[94:97]
	v_mfma_f32_16x16x32_bf16 v[90:93], v[138:141], v[196:199], v[90:93]
	s_waitcnt lgkmcnt(1)
	v_mfma_f32_16x16x32_bf16 v[78:81], v[130:133], v[204:207], v[78:81]
	v_mfma_f32_16x16x32_bf16 v[74:77], v[138:141], v[204:207], v[74:77]
	v_mfma_f32_16x16x32_bf16 v[126:129], v[134:137], v[184:187], v[126:129]
	v_mfma_f32_16x16x32_bf16 v[122:125], v[142:145], v[184:187], v[122:125]
	v_mfma_f32_16x16x32_bf16 v[110:113], v[134:137], v[192:195], v[110:113]
	v_mfma_f32_16x16x32_bf16 v[106:109], v[142:145], v[192:195], v[106:109]
	v_mfma_f32_16x16x32_bf16 v[94:97], v[134:137], v[200:203], v[94:97]
	v_mfma_f32_16x16x32_bf16 v[90:93], v[142:145], v[200:203], v[90:93]
	s_waitcnt lgkmcnt(0)
	v_mfma_f32_16x16x32_bf16 v[78:81], v[134:137], v[208:211], v[78:81]
	v_mfma_f32_16x16x32_bf16 v[74:77], v[142:145], v[208:211], v[74:77]
	s_setprio 0
	s_setprio 1
	v_mfma_f32_16x16x32_bf16 v[118:121], v[148:151], v[166:169], v[118:121]
	v_mfma_f32_16x16x32_bf16 v[114:117], v[156:159], v[166:169], v[114:117]
	v_mfma_f32_16x16x32_bf16 v[102:105], v[148:151], v[188:191], v[102:105]
	v_mfma_f32_16x16x32_bf16 v[98:101], v[156:159], v[188:191], v[98:101]
	v_mfma_f32_16x16x32_bf16 v[86:89], v[148:151], v[196:199], v[86:89]
	v_mfma_f32_16x16x32_bf16 v[82:85], v[156:159], v[196:199], v[82:85]
	v_mfma_f32_16x16x32_bf16 v[70:73], v[148:151], v[204:207], v[70:73]
	v_mfma_f32_16x16x32_bf16 v[66:69], v[156:159], v[204:207], v[66:69]
	v_mfma_f32_16x16x32_bf16 v[118:121], v[152:155], v[184:187], v[118:121]
	v_mfma_f32_16x16x32_bf16 v[114:117], v[162:165], v[184:187], v[114:117]
	v_mfma_f32_16x16x32_bf16 v[102:105], v[152:155], v[192:195], v[102:105]
	v_mfma_f32_16x16x32_bf16 v[98:101], v[162:165], v[192:195], v[98:101]
	v_mfma_f32_16x16x32_bf16 v[86:89], v[152:155], v[200:203], v[86:89]
	v_mfma_f32_16x16x32_bf16 v[82:85], v[162:165], v[200:203], v[82:85]
	v_mfma_f32_16x16x32_bf16 v[70:73], v[152:155], v[208:211], v[70:73]
	v_mfma_f32_16x16x32_bf16 v[66:69], v[162:165], v[208:211], v[66:69]
	s_setprio 0
	s_barrier
; #define PG8_STAGEB(bufoff, gbase) PG8_STAGE2(bufoff, gbase, voffB[0], voffB[1])
; #define PG8_STAGEAS(bufoff, gbase, h) PG8_STAGE2(bufoff, gbase, voffA[h][0], voffA[h][1])
; #define PG8_LDA(dst, b, h) do { _Pragma("unroll") for (int m = 0; m < 4; ++m) _Pragma("unroll") for (int k = 0; k < 2; ++k) dst[m][k] = *(const LAS bf16x8*)(lds + PG8_SA(b, h) + aoff + m * 2048 + k * 1024); } while (0)
; #define PG8_WAIT_K() do { if constexpr (HM) PG8_WAIT_V(6); else PG8_WAIT_V(8); } while (0)
; #define PG8_WAIT_L(n) asm volatile("s_waitcnt lgkmcnt(" #n ")" ::: "memory")
; #define PG8_BAR __builtin_amdgcn_s_barrier()
; #define PG8_SCHED __builtin_amdgcn_sched_barrier(0)
;     ...
;             if constexpr (!HM) PG8_LDA(At, 1, 1);
;             PG8_STAGEB(PG8_SB(1, 0), b3); PG8_STAGEB(PG8_SB(1, 1), b3 + hstepB); PG8_STAGEAS(PG8_SA(1, 0), a3, 0);
;             PG8_WAIT_K(); PG8_WAIT_L(0); PG8_BAR; if constexpr (!HM) { PG8_MMA(1, 0, At, B0); PG8_MMA(1, 1, At, B1); } PG8_BAR; PG8_SCHED;
;         }
	ds_read_b128 v[166:169], v182 offset:49152
	ds_read_b128 v[184:187], v182 offset:50176
	s_mov_b32 s34, m0
	s_mov_b32 m0, s47
	s_nop 0
	global_load_lds_dwordx4 v1, s[30:31]
	s_mov_b32 m0, s34
	ds_read_b128 v[188:191], v182 offset:51200
	ds_read_b128 v[192:195], v182 offset:52224
	s_add_u32 s26, s26, 0x80080
	s_mov_b32 s34, m0
	s_mov_b32 m0, s48
	s_nop 0
	global_load_lds_dwordx4 v172, s[30:31]
	s_mov_b32 m0, s34
	ds_read_b128 v[196:199], v182 offset:53248
	ds_read_b128 v[200:203], v182 offset:54272
	s_addc_u32 s27, s27, 0
	s_mov_b32 s30, m0
	s_mov_b32 m0, s51
	s_nop 0
	global_load_lds_dwordx4 v1, s[26:27]
	s_mov_b32 m0, s30
	ds_read_b128 v[204:207], v182 offset:55296
	ds_read_b128 v[208:211], v182 offset:56320
	s_nop 0
	s_mov_b32 s30, m0
	s_mov_b32 m0, s52
	s_nop 0
	global_load_lds_dwordx4 v172, s[26:27]
	s_mov_b32 m0, s30
	s_mov_b32 s26, m0
	s_mov_b32 m0, s49
	s_nop 0
	global_load_lds_dwordx4 v173, s[24:25]
	s_mov_b32 m0, s26
	s_nop 0
	s_mov_b32 s26, m0
	s_mov_b32 m0, s50
	s_nop 0
	global_load_lds_dwordx4 v174, s[24:25]
	s_mov_b32 m0, s26
	s_waitcnt vmcnt(8)
	s_waitcnt lgkmcnt(0)
	s_barrier
	s_setprio 1
	s_waitcnt lgkmcnt(7)
	v_mfma_f32_16x16x32_bf16 v[62:65], v[130:133], v[166:169], v[62:65]
	v_mfma_f32_16x16x32_bf16 v[58:61], v[138:141], v[166:169], v[58:61]
	s_waitcnt lgkmcnt(5)
	v_mfma_f32_16x16x32_bf16 v[46:49], v[130:133], v[188:191], v[46:49]
	v_mfma_f32_16x16x32_bf16 v[42:45], v[138:141], v[188:191], v[42:45]
	s_waitcnt lgkmcnt(3)
	v_mfma_f32_16x16x32_bf16 v[30:33], v[130:133], v[196:199], v[30:33]
	v_mfma_f32_16x16x32_bf16 v[26:29], v[138:141], v[196:199], v[26:29]
	s_waitcnt lgkmcnt(1)
	v_mfma_f32_16x16x32_bf16 v[14:17], v[130:133], v[204:207], v[14:17]
	v_mfma_f32_16x16x32_bf16 v[10:13], v[138:141], v[204:207], v[10:13]
	v_mfma_f32_16x16x32_bf16 v[62:65], v[134:137], v[184:187], v[62:65]
	v_mfma_f32_16x16x32_bf16 v[58:61], v[142:145], v[184:187], v[58:61]
	v_mfma_f32_16x16x32_bf16 v[46:49], v[134:137], v[192:195], v[46:49]
	v_mfma_f32_16x16x32_bf16 v[42:45], v[142:145], v[192:195], v[42:45]
	v_mfma_f32_16x16x32_bf16 v[30:33], v[134:137], v[200:203], v[30:33]
	v_mfma_f32_16x16x32_bf16 v[26:29], v[142:145], v[200:203], v[26:29]
	s_waitcnt lgkmcnt(0)
	v_mfma_f32_16x16x32_bf16 v[14:17], v[134:137], v[208:211], v[14:17]
	v_mfma_f32_16x16x32_bf16 v[10:13], v[142:145], v[208:211], v[10:13]
	s_setprio 0
	s_setprio 1
	v_mfma_f32_16x16x32_bf16 v[54:57], v[148:151], v[166:169], v[54:57]
	v_mfma_f32_16x16x32_bf16 v[50:53], v[156:159], v[166:169], v[50:53]
	v_mfma_f32_16x16x32_bf16 v[38:41], v[148:151], v[188:191], v[38:41]
	v_mfma_f32_16x16x32_bf16 v[34:37], v[156:159], v[188:191], v[34:37]
	v_mfma_f32_16x16x32_bf16 v[22:25], v[148:151], v[196:199], v[22:25]
	v_mfma_f32_16x16x32_bf16 v[18:21], v[156:159], v[196:199], v[18:21]
	v_mfma_f32_16x16x32_bf16 v[6:9], v[148:151], v[204:207], v[6:9]
	v_mfma_f32_16x16x32_bf16 v[2:5], v[156:159], v[204:207], v[2:5]
	v_mfma_f32_16x16x32_bf16 v[54:57], v[152:155], v[184:187], v[54:57]
	v_mfma_f32_16x16x32_bf16 v[50:53], v[162:165], v[184:187], v[50:53]
	v_mfma_f32_16x16x32_bf16 v[38:41], v[152:155], v[192:195], v[38:41]
	v_mfma_f32_16x16x32_bf16 v[34:37], v[162:165], v[192:195], v[34:37]
	v_mfma_f32_16x16x32_bf16 v[22:25], v[152:155], v[200:203], v[22:25]
	v_mfma_f32_16x16x32_bf16 v[18:21], v[162:165], v[200:203], v[18:21]
	v_mfma_f32_16x16x32_bf16 v[6:9], v[152:155], v[208:211], v[6:9]
	v_mfma_f32_16x16x32_bf16 v[2:5], v[162:165], v[208:211], v[2:5]
	s_setprio 0
	s_barrier
	s_add_i32 s59, s59, 2
	s_add_u32 s17, s17, 0x100
	s_addc_u32 s19, s19, 0
	s_add_u32 s57, s57, 0x100
	s_addc_u32 s58, s58, 0
	s_add_u32 s28, s28, 0x100
	s_addc_u32 s29, s29, 0
	s_cmp_gt_u32 s59, 29
	s_cbranch_scc0 .LBB0_611
	s_and_b64 vcc, exec, s[14:15]
	s_cbranch_vccz .LBB0_614
	s_barrier

; #define LAS __attribute__((address_space(3)))
; #define PG8_STAGEB(bufoff, gbase) PG8_STAGE2(bufoff, gbase, voffB[0], voffB[1])
; #define PG8_STAGEA(bufoff, gbase, h) PG8_STAGE2(bufoff, gbase, voffA[h][0], voffA[h][1])
; #define PG8_STAGEAS(bufoff, gbase, h) PG8_STAGE2(bufoff, gbase, voffA[h][0], voffA[h][1])
; #define PG8_LDA(dst, b, h) do { _Pragma("unroll") for (int m = 0; m < 4; ++m) _Pragma("unroll") for (int k = 0; k < 2; ++k) dst[m][k] = *(const LAS bf16x8*)(lds + PG8_SA(b, h) + aoff + m * 2048 + k * 1024); } while (0)
; #define PG8_LDB(dst, b, h) do { _Pragma("unroll") for (int n = 0; n < 2; ++n) _Pragma("unroll") for (int k = 0; k < 2; ++k) dst[n][k] = *(const LAS bf16x8*)(lds + PG8_SB(b, h) + boff + n * 2048 + k * 1024); } while (0)
; #define PG8_WAIT_K0() do { if (EST > 0 && t == 0 && ui > 0) asm volatile("s_waitcnt vmcnt(%0)" :: "n"((HM ? 6 : 8) + EST) : "memory"); else PG8_WAIT_K(); } while (0)
; #define PG8_WAIT_L(n) asm volatile("s_waitcnt lgkmcnt(" #n ")" ::: "memory")
; #define PG8_BAR __builtin_amdgcn_s_barrier()
; #define PG8_SCHED __builtin_amdgcn_sched_barrier(0)
;     ...
;             PG8_LDB(B0, 0, 0); PG8_LDB(B1, 0, 1); PG8_SCHED; PG8_LDA(At, 0, 0); if constexpr (!HM) PG8_STAGEA(PG8_SA(1, 1), a1, 1);
;             if constexpr (Sched::kGather) { if (last && has_next) { const u32x4 tn = *(const LAS u32x4*)(S.aux + tid * 16); voffA[0][0] = tn.x; voffA[0][1] = tn.y; voffA[1][0] = tn.z; voffA[1][1] = tn.w; } }
;             PG8_WAIT_K0(); PG8_WAIT_L(0); PG8_BAR; PG8_MMA(0, 0, At, B0); PG8_MMA(0, 1, At, B1); PG8_BAR; PG8_SCHED;
;             if constexpr (!HM) PG8_LDA(At, 0, 1);
;             PG8_STAGEB(PG8_SB(0, 0), b2); PG8_STAGEB(PG8_SB(0, 1), b2 + hstepB); PG8_STAGEAS(PG8_SA(0, 0), a2, 0);
.LBB0_698:
	ds_read_b128 v[130:133], v208
	ds_read_b128 v[134:137], v208 offset:1024
	ds_read_b128 v[138:141], v208 offset:2048
	ds_read_b128 v[142:145], v208 offset:3072
	ds_read_b128 v[148:151], v209
	ds_read_b128 v[152:155], v209 offset:1024
	ds_read_b128 v[156:159], v209 offset:2048
	ds_read_b128 v[160:163], v209 offset:3072
	s_cmp_eq_u32 s63, 28
	s_cselect_b32 s38, s0, s19
	s_cselect_b32 s39, s1, s21
	s_cselect_b32 s34, s22, s25
	s_cselect_b32 s35, s23, s27
	s_add_u32 s30, s38, 0x80
	s_addc_u32 s31, s39, 0
	ds_read_b128 v[164:167], v210
	ds_read_b128 v[168:171], v210 offset:1024
	ds_read_b128 v[172:175], v210 offset:2048
	ds_read_b128 v[176:179], v210 offset:3072
	ds_read_b128 v[182:185], v210 offset:4096
	ds_read_b128 v[186:189], v210 offset:5120
	ds_read_b128 v[190:193], v210 offset:6144
	ds_read_b128 v[194:197], v210 offset:7168
	s_mov_b32 s64, m0
	s_mov_b32 m0, s58
	s_nop 0
	global_load_lds_dwordx4 v203, s[28:29]
	s_mov_b32 m0, s64
	s_add_u32 s36, s34, 0x80
	s_mov_b32 s64, m0
	s_mov_b32 m0, s59
	s_nop 0
	global_load_lds_dwordx4 v204, s[28:29]
	s_mov_b32 m0, s64
	s_waitcnt vmcnt(8)
	s_waitcnt lgkmcnt(0)
	s_addc_u32 s37, s35, 0
	s_barrier
	s_setprio 1
	s_waitcnt lgkmcnt(7)
	v_mfma_f32_16x16x32_bf16 v[126:129], v[130:133], v[164:167], v[126:129]
	v_mfma_f32_16x16x32_bf16 v[118:121], v[138:141], v[164:167], v[118:121]
	s_waitcnt lgkmcnt(5)
	v_mfma_f32_16x16x32_bf16 v[110:113], v[130:133], v[172:175], v[110:113]
	v_mfma_f32_16x16x32_bf16 v[102:105], v[138:141], v[172:175], v[102:105]
	s_waitcnt lgkmcnt(3)
	v_mfma_f32_16x16x32_bf16 v[94:97], v[130:133], v[182:185], v[94:97]
	v_mfma_f32_16x16x32_bf16 v[86:89], v[138:141], v[182:185], v[86:89]
	s_waitcnt lgkmcnt(1)
	v_mfma_f32_16x16x32_bf16 v[78:81], v[130:133], v[190:193], v[78:81]
	v_mfma_f32_16x16x32_bf16 v[70:73], v[138:141], v[190:193], v[70:73]
	v_mfma_f32_16x16x32_bf16 v[126:129], v[134:137], v[168:171], v[126:129]
	v_mfma_f32_16x16x32_bf16 v[118:121], v[142:145], v[168:171], v[118:121]
	v_mfma_f32_16x16x32_bf16 v[110:113], v[134:137], v[176:179], v[110:113]
	v_mfma_f32_16x16x32_bf16 v[102:105], v[142:145], v[176:179], v[102:105]
	v_mfma_f32_16x16x32_bf16 v[94:97], v[134:137], v[186:189], v[94:97]
	v_mfma_f32_16x16x32_bf16 v[86:89], v[142:145], v[186:189], v[86:89]
	s_waitcnt lgkmcnt(0)
	v_mfma_f32_16x16x32_bf16 v[78:81], v[134:137], v[194:197], v[78:81]
	v_mfma_f32_16x16x32_bf16 v[70:73], v[142:145], v[194:197], v[70:73]
	s_setprio 0
	s_setprio 1
	v_mfma_f32_16x16x32_bf16 v[122:125], v[148:151], v[164:167], v[122:125]
	v_mfma_f32_16x16x32_bf16 v[114:117], v[156:159], v[164:167], v[114:117]
	v_mfma_f32_16x16x32_bf16 v[106:109], v[148:151], v[172:175], v[106:109]
	v_mfma_f32_16x16x32_bf16 v[98:101], v[156:159], v[172:175], v[98:101]
	v_mfma_f32_16x16x32_bf16 v[90:93], v[148:151], v[182:185], v[90:93]
	v_mfma_f32_16x16x32_bf16 v[82:85], v[156:159], v[182:185], v[82:85]
	v_mfma_f32_16x16x32_bf16 v[74:77], v[148:151], v[190:193], v[74:77]
	v_mfma_f32_16x16x32_bf16 v[66:69], v[156:159], v[190:193], v[66:69]
	v_mfma_f32_16x16x32_bf16 v[122:125], v[152:155], v[168:171], v[122:125]
	v_mfma_f32_16x16x32_bf16 v[114:117], v[160:163], v[168:171], v[114:117]
	v_mfma_f32_16x16x32_bf16 v[106:109], v[152:155], v[176:179], v[106:109]
	v_mfma_f32_16x16x32_bf16 v[98:101], v[160:163], v[176:179], v[98:101]
	v_mfma_f32_16x16x32_bf16 v[90:93], v[152:155], v[186:189], v[90:93]
	v_mfma_f32_16x16x32_bf16 v[82:85], v[160:163], v[186:189], v[82:85]
	v_mfma_f32_16x16x32_bf16 v[74:77], v[152:155], v[194:197], v[74:77]
	v_mfma_f32_16x16x32_bf16 v[66:69], v[160:163], v[194:197], v[66:69]
	s_setprio 0
	s_barrier
	ds_read_b128 v[164:167], v210 offset:16384
	ds_read_b128 v[168:171], v210 offset:17408
	s_mov_b32 s64, m0
	s_mov_b32 m0, s43
	s_nop 0
	global_load_lds_dwordx4 v1, s[34:35]
	s_mov_b32 m0, s64
	ds_read_b128 v[172:175], v210 offset:18432
	ds_read_b128 v[176:179], v210 offset:19456
	s_nop 0
	s_mov_b32 s64, m0
	s_mov_b32 m0, s44
	s_nop 0
	global_load_lds_dwordx4 v200, s[34:35]
	s_mov_b32 m0, s64
	ds_read_b128 v[182:185], v210 offset:20480
	ds_read_b128 v[186:189], v210 offset:21504
	s_add_u32 s64, s34, 0x80000
	s_addc_u32 s65, s35, 0
	s_mov_b32 s66, m0
	s_mov_b32 m0, s45
	s_nop 0
	global_load_lds_dwordx4 v1, s[64:65]
	s_mov_b32 m0, s66
	ds_read_b128 v[190:193], v210 offset:22528
	ds_read_b128 v[194:197], v210 offset:23552
	s_nop 0
	s_mov_b32 s66, m0
	s_mov_b32 m0, s46
	s_nop 0
	global_load_lds_dwordx4 v200, s[64:65]
	s_mov_b32 m0, s66
	s_mov_b32 s64, m0
	s_mov_b32 m0, s42
	s_nop 0
	global_load_lds_dwordx4 v201, s[38:39]
	s_mov_b32 m0, s64
	s_nop 0
	s_mov_b32 s64, m0
	s_mov_b32 m0, s47
	s_nop 0
	global_load_lds_dwordx4 v202, s[38:39]
	s_mov_b32 m0, s64
	s_waitcnt vmcnt(8)
	s_waitcnt lgkmcnt(0)
	s_barrier
; #define PG8_STAGEAS(bufoff, gbase, h) PG8_STAGE2(bufoff, gbase, voffA[h][0], voffA[h][1])
; #define PG8_LDA(dst, b, h) do { _Pragma("unroll") for (int m = 0; m < 4; ++m) _Pragma("unroll") for (int k = 0; k < 2; ++k) dst[m][k] = *(const LAS bf16x8*)(lds + PG8_SA(b, h) + aoff + m * 2048 + k * 1024); } while (0)
; #define PG8_LDB(dst, b, h) do { _Pragma("unroll") for (int n = 0; n < 2; ++n) _Pragma("unroll") for (int k = 0; k < 2; ++k) dst[n][k] = *(const LAS bf16x8*)(lds + PG8_SB(b, h) + boff + n * 2048 + k * 1024); } while (0)
; #define PG8_WAIT_K() do { if constexpr (HM) PG8_WAIT_V(6); else PG8_WAIT_V(8); } while (0)
; #define PG8_WAIT_K0() do { if (EST > 0 && t == 0 && ui > 0) asm volatile("s_waitcnt vmcnt(%0)" :: "n"((HM ? 6 : 8) + EST) : "memory"); else PG8_WAIT_K(); } while (0)
; #define PG8_WAIT_L(n) asm volatile("s_waitcnt lgkmcnt(" #n ")" ::: "memory")
; #define PG8_BAR __builtin_amdgcn_s_barrier()
; #define PG8_SCHED __builtin_amdgcn_sched_barrier(0)
;     ...
;             PG8_WAIT_K0(); PG8_WAIT_L(0); PG8_BAR; if constexpr (!HM) { PG8_MMA(1, 0, At, B0); PG8_MMA(1, 1, At, B1); } PG8_BAR; PG8_SCHED;
;             PG8_LDB(B0, 1, 0); PG8_LDB(B1, 1, 1); PG8_SCHED; PG8_LDA(At, 1, 0); if constexpr (!HM) PG8_STAGEAS(PG8_SA(0, 1), a2, 1);
;             PG8_WAIT_K(); PG8_WAIT_L(0); PG8_BAR; PG8_MMA(0, 0, At, B0); PG8_MMA(0, 1, At, B1); PG8_BAR; PG8_SCHED;
	s_setprio 1
	s_waitcnt lgkmcnt(7)
	v_mfma_f32_16x16x32_bf16 v[62:65], v[130:133], v[164:167], v[62:65]
	v_mfma_f32_16x16x32_bf16 v[54:57], v[138:141], v[164:167], v[54:57]
	s_waitcnt lgkmcnt(5)
	v_mfma_f32_16x16x32_bf16 v[46:49], v[130:133], v[172:175], v[46:49]
	v_mfma_f32_16x16x32_bf16 v[38:41], v[138:141], v[172:175], v[38:41]
	s_waitcnt lgkmcnt(3)
	v_mfma_f32_16x16x32_bf16 v[30:33], v[130:133], v[182:185], v[30:33]
	v_mfma_f32_16x16x32_bf16 v[22:25], v[138:141], v[182:185], v[22:25]
	s_waitcnt lgkmcnt(1)
	v_mfma_f32_16x16x32_bf16 v[14:17], v[130:133], v[190:193], v[14:17]
	v_mfma_f32_16x16x32_bf16 v[6:9], v[138:141], v[190:193], v[6:9]
	v_mfma_f32_16x16x32_bf16 v[62:65], v[134:137], v[168:171], v[62:65]
	v_mfma_f32_16x16x32_bf16 v[54:57], v[142:145], v[168:171], v[54:57]
	v_mfma_f32_16x16x32_bf16 v[46:49], v[134:137], v[176:179], v[46:49]
	v_mfma_f32_16x16x32_bf16 v[38:41], v[142:145], v[176:179], v[38:41]
	v_mfma_f32_16x16x32_bf16 v[30:33], v[134:137], v[186:189], v[30:33]
	v_mfma_f32_16x16x32_bf16 v[22:25], v[142:145], v[186:189], v[22:25]
	s_waitcnt lgkmcnt(0)
	v_mfma_f32_16x16x32_bf16 v[14:17], v[134:137], v[194:197], v[14:17]
	v_mfma_f32_16x16x32_bf16 v[6:9], v[142:145], v[194:197], v[6:9]
	s_setprio 0
	s_setprio 1
	v_mfma_f32_16x16x32_bf16 v[58:61], v[148:151], v[164:167], v[58:61]
	v_mfma_f32_16x16x32_bf16 v[50:53], v[156:159], v[164:167], v[50:53]
	v_mfma_f32_16x16x32_bf16 v[42:45], v[148:151], v[172:175], v[42:45]
	v_mfma_f32_16x16x32_bf16 v[34:37], v[156:159], v[172:175], v[34:37]
	v_mfma_f32_16x16x32_bf16 v[26:29], v[148:151], v[182:185], v[26:29]
	v_mfma_f32_16x16x32_bf16 v[18:21], v[156:159], v[182:185], v[18:21]
	v_mfma_f32_16x16x32_bf16 v[10:13], v[148:151], v[190:193], v[10:13]
	v_mfma_f32_16x16x32_bf16 v[2:5], v[156:159], v[190:193], v[2:5]
	v_mfma_f32_16x16x32_bf16 v[58:61], v[152:155], v[168:171], v[58:61]
	v_mfma_f32_16x16x32_bf16 v[50:53], v[160:163], v[168:171], v[50:53]
	v_mfma_f32_16x16x32_bf16 v[42:45], v[152:155], v[176:179], v[42:45]
	v_mfma_f32_16x16x32_bf16 v[34:37], v[160:163], v[176:179], v[34:37]
	v_mfma_f32_16x16x32_bf16 v[26:29], v[152:155], v[186:189], v[26:29]
	v_mfma_f32_16x16x32_bf16 v[18:21], v[160:163], v[186:189], v[18:21]
	v_mfma_f32_16x16x32_bf16 v[10:13], v[152:155], v[194:197], v[10:13]
	v_mfma_f32_16x16x32_bf16 v[2:5], v[160:163], v[194:197], v[2:5]
	s_setprio 0
	s_barrier
	ds_read_b128 v[130:133], v146
	ds_read_b128 v[134:137], v146 offset:1024
	ds_read_b128 v[138:141], v146 offset:2048
	ds_read_b128 v[142:145], v146 offset:3072
	ds_read_b128 v[148:151], v147
	ds_read_b128 v[152:155], v147 offset:1024
	ds_read_b128 v[156:159], v147 offset:2048
	ds_read_b128 v[160:163], v147 offset:3072
	ds_read_b128 v[164:167], v210 offset:32768
	ds_read_b128 v[168:171], v210 offset:33792
	ds_read_b128 v[172:175], v210 offset:34816
	ds_read_b128 v[176:179], v210 offset:35840
	ds_read_b128 v[182:185], v210 offset:36864
	ds_read_b128 v[186:189], v210 offset:37888
	ds_read_b128 v[190:193], v210 offset:38912
	ds_read_b128 v[194:197], v210 offset:39936
	s_mov_b32 s64, m0
	s_mov_b32 m0, s48
	s_nop 0
	global_load_lds_dwordx4 v203, s[38:39]
	s_mov_b32 m0, s64
	s_nop 0
	s_mov_b32 s64, m0
	s_mov_b32 m0, s49
	s_nop 0
	global_load_lds_dwordx4 v204, s[38:39]
	s_mov_b32 m0, s64
	s_waitcnt vmcnt(8)
	s_waitcnt lgkmcnt(0)
	s_barrier
	s_setprio 1
	s_waitcnt lgkmcnt(7)
	v_mfma_f32_16x16x32_bf16 v[126:129], v[130:133], v[164:167], v[126:129]
	v_mfma_f32_16x16x32_bf16 v[118:121], v[138:141], v[164:167], v[118:121]
	s_waitcnt lgkmcnt(5)
	v_mfma_f32_16x16x32_bf16 v[110:113], v[130:133], v[172:175], v[110:113]
	v_mfma_f32_16x16x32_bf16 v[102:105], v[138:141], v[172:175], v[102:105]
	s_waitcnt lgkmcnt(3)
	v_mfma_f32_16x16x32_bf16 v[94:97], v[130:133], v[182:185], v[94:97]
	v_mfma_f32_16x16x32_bf16 v[86:89], v[138:141], v[182:185], v[86:89]
	s_waitcnt lgkmcnt(1)
	v_mfma_f32_16x16x32_bf16 v[78:81], v[130:133], v[190:193], v[78:81]
	v_mfma_f32_16x16x32_bf16 v[70:73], v[138:141], v[190:193], v[70:73]
	v_mfma_f32_16x16x32_bf16 v[126:129], v[134:137], v[168:171], v[126:129]
	v_mfma_f32_16x16x32_bf16 v[118:121], v[142:145], v[168:171], v[118:121]
	v_mfma_f32_16x16x32_bf16 v[110:113], v[134:137], v[176:179], v[110:113]
	v_mfma_f32_16x16x32_bf16 v[102:105], v[142:145], v[176:179], v[102:105]
	v_mfma_f32_16x16x32_bf16 v[94:97], v[134:137], v[186:189], v[94:97]
	v_mfma_f32_16x16x32_bf16 v[86:89], v[142:145], v[186:189], v[86:89]
	s_waitcnt lgkmcnt(0)
	v_mfma_f32_16x16x32_bf16 v[78:81], v[134:137], v[194:197], v[78:81]
	v_mfma_f32_16x16x32_bf16 v[70:73], v[142:145], v[194:197], v[70:73]
	s_setprio 0
	s_setprio 1
	v_mfma_f32_16x16x32_bf16 v[122:125], v[148:151], v[164:167], v[122:125]
	v_mfma_f32_16x16x32_bf16 v[114:117], v[156:159], v[164:167], v[114:117]
	v_mfma_f32_16x16x32_bf16 v[106:109], v[148:151], v[172:175], v[106:109]
	v_mfma_f32_16x16x32_bf16 v[98:101], v[156:159], v[172:175], v[98:101]
	v_mfma_f32_16x16x32_bf16 v[90:93], v[148:151], v[182:185], v[90:93]
	v_mfma_f32_16x16x32_bf16 v[82:85], v[156:159], v[182:185], v[82:85]
	v_mfma_f32_16x16x32_bf16 v[74:77], v[148:151], v[190:193], v[74:77]
	v_mfma_f32_16x16x32_bf16 v[66:69], v[156:159], v[190:193], v[66:69]
	v_mfma_f32_16x16x32_bf16 v[122:125], v[152:155], v[168:171], v[122:125]
	v_mfma_f32_16x16x32_bf16 v[114:117], v[160:163], v[168:171], v[114:117]
	v_mfma_f32_16x16x32_bf16 v[106:109], v[152:155], v[176:179], v[106:109]
	v_mfma_f32_16x16x32_bf16 v[98:101], v[160:163], v[176:179], v[98:101]
	v_mfma_f32_16x16x32_bf16 v[90:93], v[152:155], v[186:189], v[90:93]
	v_mfma_f32_16x16x32_bf16 v[82:85], v[160:163], v[186:189], v[82:85]
	v_mfma_f32_16x16x32_bf16 v[74:77], v[152:155], v[194:197], v[74:77]
	v_mfma_f32_16x16x32_bf16 v[66:69], v[160:163], v[194:197], v[66:69]
	s_setprio 0
	s_barrier
; #define PG8_STAGEB(bufoff, gbase) PG8_STAGE2(bufoff, gbase, voffB[0], voffB[1])
; #define PG8_STAGEAS(bufoff, gbase, h) PG8_STAGE2(bufoff, gbase, voffA[h][0], voffA[h][1])
; #define PG8_LDA(dst, b, h) do { _Pragma("unroll") for (int m = 0; m < 4; ++m) _Pragma("unroll") for (int k = 0; k < 2; ++k) dst[m][k] = *(const LAS bf16x8*)(lds + PG8_SA(b, h) + aoff + m * 2048 + k * 1024); } while (0)
; #define PG8_WAIT_K() do { if constexpr (HM) PG8_WAIT_V(6); else PG8_WAIT_V(8); } while (0)
; #define PG8_WAIT_L(n) asm volatile("s_waitcnt lgkmcnt(" #n ")" ::: "memory")
; #define PG8_BAR __builtin_amdgcn_s_barrier()
; #define PG8_SCHED __builtin_amdgcn_sched_barrier(0)
;     ...
;             if constexpr (!HM) PG8_LDA(At, 1, 1);
;             PG8_STAGEB(PG8_SB(1, 0), b3); PG8_STAGEB(PG8_SB(1, 1), b3 + hstepB); PG8_STAGEAS(PG8_SA(1, 0), a3, 0);
;             PG8_WAIT_K(); PG8_WAIT_L(0); PG8_BAR; if constexpr (!HM) { PG8_MMA(1, 0, At, B0); PG8_MMA(1, 1, At, B1); } PG8_BAR; PG8_SCHED;
;         }
;         if (wr == 0) PG8_BAR;
	ds_read_b128 v[164:167], v210 offset:49152
	ds_read_b128 v[168:171], v210 offset:50176
	s_mov_b32 s38, m0
	s_mov_b32 m0, s52
	s_nop 0
	global_load_lds_dwordx4 v1, s[36:37]
	s_mov_b32 m0, s38
	ds_read_b128 v[172:175], v210 offset:51200
	ds_read_b128 v[176:179], v210 offset:52224
	s_add_u32 s34, s34, 0x80080
	s_mov_b32 s38, m0
	s_mov_b32 m0, s53
	s_nop 0
	global_load_lds_dwordx4 v200, s[36:37]
	s_mov_b32 m0, s38
	ds_read_b128 v[182:185], v210 offset:53248
	ds_read_b128 v[186:189], v210 offset:54272
	s_addc_u32 s35, s35, 0
	s_mov_b32 s36, m0
	s_mov_b32 m0, s56
	s_nop 0
	global_load_lds_dwordx4 v1, s[34:35]
	s_mov_b32 m0, s36
	ds_read_b128 v[190:193], v210 offset:55296
	ds_read_b128 v[194:197], v210 offset:56320
	s_nop 0
	s_mov_b32 s36, m0
	s_mov_b32 m0, s57
	s_nop 0
	global_load_lds_dwordx4 v200, s[34:35]
	s_mov_b32 m0, s36
	s_mov_b32 s34, m0
	s_mov_b32 m0, s54
	s_nop 0
	global_load_lds_dwordx4 v201, s[30:31]
	s_mov_b32 m0, s34
	s_nop 0
	s_mov_b32 s34, m0
	s_mov_b32 m0, s55
	s_nop 0
	global_load_lds_dwordx4 v202, s[30:31]
	s_mov_b32 m0, s34
	s_waitcnt vmcnt(8)
	s_waitcnt lgkmcnt(0)
	s_barrier
	s_setprio 1
	s_waitcnt lgkmcnt(7)
	v_mfma_f32_16x16x32_bf16 v[62:65], v[130:133], v[164:167], v[62:65]
	v_mfma_f32_16x16x32_bf16 v[54:57], v[138:141], v[164:167], v[54:57]
	s_waitcnt lgkmcnt(5)
	v_mfma_f32_16x16x32_bf16 v[46:49], v[130:133], v[172:175], v[46:49]
	v_mfma_f32_16x16x32_bf16 v[38:41], v[138:141], v[172:175], v[38:41]
	s_waitcnt lgkmcnt(3)
	v_mfma_f32_16x16x32_bf16 v[30:33], v[130:133], v[182:185], v[30:33]
	v_mfma_f32_16x16x32_bf16 v[22:25], v[138:141], v[182:185], v[22:25]
	s_waitcnt lgkmcnt(1)
	v_mfma_f32_16x16x32_bf16 v[14:17], v[130:133], v[190:193], v[14:17]
	v_mfma_f32_16x16x32_bf16 v[6:9], v[138:141], v[190:193], v[6:9]
	v_mfma_f32_16x16x32_bf16 v[62:65], v[134:137], v[168:171], v[62:65]
	v_mfma_f32_16x16x32_bf16 v[54:57], v[142:145], v[168:171], v[54:57]
	v_mfma_f32_16x16x32_bf16 v[46:49], v[134:137], v[176:179], v[46:49]
	v_mfma_f32_16x16x32_bf16 v[38:41], v[142:145], v[176:179], v[38:41]
	v_mfma_f32_16x16x32_bf16 v[30:33], v[134:137], v[186:189], v[30:33]
	v_mfma_f32_16x16x32_bf16 v[22:25], v[142:145], v[186:189], v[22:25]
	s_waitcnt lgkmcnt(0)
	v_mfma_f32_16x16x32_bf16 v[14:17], v[134:137], v[194:197], v[14:17]
	v_mfma_f32_16x16x32_bf16 v[6:9], v[142:145], v[194:197], v[6:9]
	s_setprio 0
	s_setprio 1
	v_mfma_f32_16x16x32_bf16 v[58:61], v[148:151], v[164:167], v[58:61]
	v_mfma_f32_16x16x32_bf16 v[50:53], v[156:159], v[164:167], v[50:53]
	v_mfma_f32_16x16x32_bf16 v[42:45], v[148:151], v[172:175], v[42:45]
	v_mfma_f32_16x16x32_bf16 v[34:37], v[156:159], v[172:175], v[34:37]
	v_mfma_f32_16x16x32_bf16 v[26:29], v[148:151], v[182:185], v[26:29]
	v_mfma_f32_16x16x32_bf16 v[18:21], v[156:159], v[182:185], v[18:21]
	v_mfma_f32_16x16x32_bf16 v[10:13], v[148:151], v[190:193], v[10:13]
	v_mfma_f32_16x16x32_bf16 v[2:5], v[156:159], v[190:193], v[2:5]
	v_mfma_f32_16x16x32_bf16 v[58:61], v[152:155], v[168:171], v[58:61]
	v_mfma_f32_16x16x32_bf16 v[50:53], v[160:163], v[168:171], v[50:53]
	v_mfma_f32_16x16x32_bf16 v[42:45], v[152:155], v[176:179], v[42:45]
	v_mfma_f32_16x16x32_bf16 v[34:37], v[160:163], v[176:179], v[34:37]
	v_mfma_f32_16x16x32_bf16 v[26:29], v[152:155], v[186:189], v[26:29]
	v_mfma_f32_16x16x32_bf16 v[18:21], v[160:163], v[186:189], v[18:21]
	v_mfma_f32_16x16x32_bf16 v[10:13], v[152:155], v[194:197], v[10:13]
	v_mfma_f32_16x16x32_bf16 v[2:5], v[160:163], v[194:197], v[2:5]
	s_setprio 0
	s_barrier
	s_add_i32 s63, s63, 2
	s_add_u32 s19, s19, 0x100
	s_addc_u32 s21, s21, 0
	s_add_u32 s25, s25, 0x100
	s_addc_u32 s27, s27, 0
	s_add_u32 s28, s28, 0x100
	s_addc_u32 s29, s29, 0
	s_cmp_gt_u32 s63, 29
	s_cbranch_scc0 .LBB0_698
	s_and_b64 vcc, exec, s[16:17]
	s_cbranch_vccz .LBB0_701
	s_barrier
